# v73 + pool_sums: window-sum chain heads 0+a then +b merged into a+b (231 fewer VALU per tile)
# baseline (speedup 1.0000x reference)
.LBB0_583:
	s_or_b64 exec, exec, s[8:9]
	s_waitcnt lgkmcnt(0)
	s_barrier
	s_load_dwordx2 s[100:101], s[0:1], 0xd0
	v_and_b32_e32 v232, 31, v234
	v_or_b32_e32 v232, s67, v232
	v_mov_b32_e32 v233, 0
	v_lshlrev_b64 v[232:233], 8, v[232:233]
	v_lshrrev_b32_e32 v248, 5, v234
	v_and_b32_e32 v248, 1, v248
	v_lshlrev_b32_e32 v248, 4, v248
	v_mov_b32_e32 v249, 0
	v_lshl_add_u64 v[232:233], v[232:233], 0, v[248:249]
	s_waitcnt lgkmcnt(0)
	v_lshl_add_u64 v[232:233], s[100:101], 0, v[232:233]
	s_mov_b32 s100, 0x1600000
	s_mov_b32 s101, 0
	v_lshl_add_u64 v[248:249], v[232:233], 0, s[100:101]
	s_mov_b32 s100, 0x1602000
	v_lshl_add_u64 v[250:251], v[232:233], 0, s[100:101]
	global_load_dwordx4 v[168:171], v[248:249], off
	global_load_dwordx4 v[172:175], v[250:251], off
	global_load_dwordx4 v[176:179], v[248:249], off offset:32
	global_load_dwordx4 v[180:183], v[250:251], off offset:32
	global_load_dwordx4 v[184:187], v[248:249], off offset:64
	global_load_dwordx4 v[188:191], v[250:251], off offset:64
	global_load_dwordx4 v[192:195], v[248:249], off offset:96
	global_load_dwordx4 v[196:199], v[250:251], off offset:96
	global_load_dwordx4 v[200:203], v[248:249], off offset:128
	global_load_dwordx4 v[204:207], v[250:251], off offset:128
	global_load_dwordx4 v[208:211], v[248:249], off offset:160
	global_load_dwordx4 v[212:215], v[250:251], off offset:160
	global_load_dwordx4 v[216:219], v[248:249], off offset:192
	global_load_dwordx4 v[220:223], v[250:251], off offset:192
	global_load_dwordx4 v[224:227], v[248:249], off offset:224
	global_load_dwordx4 v[228:231], v[250:251], off offset:224
	v_mbcnt_lo_u32_b32 v0, -1, 0
	v_mbcnt_hi_u32_b32 v0, -1, v0
	s_and_b32 s5, s34, 31
	v_add_u32_e32 v114, s67, v0
	s_cmp_eq_u32 s5, 0
	v_lshl_add_u32 v0, v114, 1, 0
	ds_read_u16 v2, v0 offset:14560
	ds_read_u16 v3, v0 offset:15600
	ds_read_u16 v4, v0 offset:16640
	ds_read_u16 v5, v0 offset:17680
	ds_read_u16 v6, v0 offset:18720
	ds_read_u16 v7, v0 offset:19760
	ds_read_u16 v8, v0 offset:20800
	ds_read_u16 v9, v0 offset:21840
	s_waitcnt lgkmcnt(7)
	v_lshlrev_b32_e32 v115, 16, v2
	s_waitcnt lgkmcnt(6)
	v_lshlrev_b32_e32 v49, 16, v3
	s_waitcnt lgkmcnt(5)
	v_lshlrev_b32_e32 v46, 16, v4
	s_waitcnt lgkmcnt(4)
	v_lshlrev_b32_e32 v43, 16, v5
	s_waitcnt lgkmcnt(3)
	v_lshlrev_b32_e32 v41, 16, v6
	s_waitcnt lgkmcnt(2)
	v_lshlrev_b32_e32 v38, 16, v7
	s_waitcnt lgkmcnt(1)
	v_lshlrev_b32_e32 v35, 16, v8
	s_waitcnt lgkmcnt(0)
	v_lshlrev_b32_e32 v32, 16, v9
	ds_read_u16 v2, v0 offset:22880
	ds_read_u16 v3, v0 offset:23920
	ds_read_u16 v4, v0 offset:24960
	ds_read_u16 v5, v0 offset:26000
	ds_read_u16 v6, v0 offset:27040
	ds_read_u16 v7, v0 offset:28080
	ds_read_u16 v8, v0 offset:29120
	ds_read_u16 v9, v0 offset:30160
	s_waitcnt lgkmcnt(7)
	v_lshlrev_b32_e32 v39, 16, v2
	s_waitcnt lgkmcnt(6)
	v_lshlrev_b32_e32 v36, 16, v3
	s_waitcnt lgkmcnt(5)
	v_lshlrev_b32_e32 v33, 16, v4
	s_waitcnt lgkmcnt(4)
	v_lshlrev_b32_e32 v29, 16, v5
	s_waitcnt lgkmcnt(3)
	v_lshlrev_b32_e32 v26, 16, v6
	v_add_u32_e32 v2, 0x10400, v0
	v_add_u32_e32 v3, 0x10810, v0
	v_add_u32_e32 v4, 0x10c20, v0
	v_add_u32_e32 v5, 0x11030, v0
	v_add_u32_e32 v6, 0x11440, v0
	s_waitcnt lgkmcnt(2)
	v_lshlrev_b32_e32 v24, 16, v7
	s_waitcnt lgkmcnt(1)
	v_lshlrev_b32_e32 v22, 16, v8
	s_waitcnt lgkmcnt(0)
	v_lshlrev_b32_e32 v20, 16, v9
	v_add_u32_e32 v7, 0x11850, v0
	ds_read_u16 v8, v0 offset:31200
	ds_read_u16 v9, v0 offset:32240
	ds_read_u16 v2, v2
	ds_read_u16 v3, v3
	ds_read_u16 v4, v4
	ds_read_u16 v5, v5
	ds_read_u16 v6, v6
	ds_read_u16 v10, v7
	s_waitcnt lgkmcnt(7)
	v_lshlrev_b32_e32 v64, 16, v8
	s_waitcnt lgkmcnt(6)
	v_lshlrev_b32_e32 v62, 16, v9
	ds_read_u16 v7, v0 offset:33280
	ds_read_u16 v8, v0 offset:34320
	ds_read_u16 v9, v0 offset:35360
	ds_read_u16 v11, v0 offset:36400
	ds_read_u16 v12, v0 offset:37440
	ds_read_u16 v13, v0 offset:38480
	ds_read_u16 v14, v0 offset:39520
	ds_read_u16 v15, v0 offset:40560
	s_waitcnt lgkmcnt(7)
	v_lshlrev_b32_e32 v65, 16, v7
	s_waitcnt lgkmcnt(6)
	v_lshlrev_b32_e32 v63, 16, v8
	s_waitcnt lgkmcnt(5)
	v_lshlrev_b32_e32 v61, 16, v9
	s_waitcnt lgkmcnt(4)
	v_lshlrev_b32_e32 v60, 16, v11
	s_waitcnt lgkmcnt(3)
	v_lshlrev_b32_e32 v59, 16, v12
	s_waitcnt lgkmcnt(2)
	v_lshlrev_b32_e32 v58, 16, v13
	s_waitcnt lgkmcnt(1)
	v_lshlrev_b32_e32 v56, 16, v14
	s_waitcnt lgkmcnt(0)
	v_lshlrev_b32_e32 v54, 16, v15
	ds_read_u16 v7, v0 offset:41600
	ds_read_u16 v8, v0 offset:42640
	ds_read_u16 v9, v0 offset:43680
	ds_read_u16 v11, v0 offset:44720
	ds_read_u16 v12, v0 offset:45760
	ds_read_u16 v13, v0 offset:46800
	ds_read_u16 v14, v0 offset:47840
	ds_read_u16 v15, v0 offset:48880
	s_waitcnt lgkmcnt(7)
	v_lshlrev_b32_e32 v57, 16, v7
	s_waitcnt lgkmcnt(6)
	v_lshlrev_b32_e32 v55, 16, v8
	s_waitcnt lgkmcnt(5)
	v_lshlrev_b32_e32 v53, 16, v9
	s_waitcnt lgkmcnt(4)
	v_lshlrev_b32_e32 v52, 16, v11
	s_waitcnt lgkmcnt(3)
	v_lshlrev_b32_e32 v51, 16, v12
	s_waitcnt lgkmcnt(2)
	v_lshlrev_b32_e32 v50, 16, v13
	s_waitcnt lgkmcnt(1)
	v_lshlrev_b32_e32 v47, 16, v14
	s_waitcnt lgkmcnt(0)
	v_lshlrev_b32_e32 v44, 16, v15
	ds_read_u16 v7, v0 offset:49920
	ds_read_u16 v8, v0 offset:50960
	ds_read_u16 v9, v0 offset:52000
	ds_read_u16 v11, v0 offset:53040
	ds_read_u16 v12, v0 offset:54080
	ds_read_u16 v13, v0 offset:55120
	ds_read_u16 v14, v0 offset:56160
	ds_read_u16 v15, v0 offset:57200
	s_waitcnt lgkmcnt(7)
	v_lshlrev_b32_e32 v48, 16, v7
	s_waitcnt lgkmcnt(6)
	v_lshlrev_b32_e32 v45, 16, v8
	s_waitcnt lgkmcnt(5)
	v_lshlrev_b32_e32 v42, 16, v9
	s_waitcnt lgkmcnt(4)
	v_lshlrev_b32_e32 v40, 16, v11
	s_waitcnt lgkmcnt(3)
	v_lshlrev_b32_e32 v37, 16, v12
	s_waitcnt lgkmcnt(2)
	v_lshlrev_b32_e32 v34, 16, v13
	s_waitcnt lgkmcnt(1)
	v_lshlrev_b32_e32 v30, 16, v14
	s_waitcnt lgkmcnt(0)
	v_lshlrev_b32_e32 v27, 16, v15
	ds_read_u16 v7, v0 offset:58240
	ds_read_u16 v8, v0 offset:59280
	ds_read_u16 v9, v0 offset:60320
	ds_read_u16 v11, v0 offset:61360
	ds_read_u16 v12, v0 offset:62400
	ds_read_u16 v13, v0 offset:63440
	ds_read_u16 v14, v0 offset:64480
	ds_read_u16 v15, v0 offset:65520
	s_waitcnt lgkmcnt(7)
	v_lshlrev_b32_e32 v31, 16, v7
	s_waitcnt lgkmcnt(6)
	v_lshlrev_b32_e32 v28, 16, v8
	s_waitcnt lgkmcnt(5)
	v_lshlrev_b32_e32 v25, 16, v9
	s_waitcnt lgkmcnt(3)
	v_lshlrev_b32_e32 v21, 16, v12
	s_waitcnt lgkmcnt(1)
	v_lshlrev_b32_e32 v18, 16, v14
	v_lshlrev_b32_e32 v14, 16, v2
	v_lshlrev_b32_e32 v12, 16, v3
	v_lshlrev_b32_e32 v9, 16, v4
	v_lshlrev_b32_e32 v7, 16, v5
	v_lshlrev_b32_e32 v5, 16, v6
	v_lshlrev_b32_e32 v3, 16, v10
	v_add_u32_e32 v2, 0x11c60, v0
	v_add_u32_e32 v4, 0x12070, v0
	v_add_u32_e32 v6, 0x12480, v0
	v_add_u32_e32 v8, 0x12890, v0
	v_add_u32_e32 v10, 0x12ca0, v0
	v_lshlrev_b32_e32 v23, 16, v11
	v_lshlrev_b32_e32 v19, 16, v13
	s_waitcnt lgkmcnt(0)
	v_lshlrev_b32_e32 v16, 16, v15
	v_add_u32_e32 v11, 0x130b0, v0
	v_add_u32_e32 v13, 0x134c0, v0
	v_add_u32_e32 v15, 0x138d0, v0
	ds_read_u16 v2, v2
	ds_read_u16 v4, v4
	ds_read_u16 v6, v6
	ds_read_u16 v8, v8
	ds_read_u16 v10, v10
	ds_read_u16 v122, v11
	ds_read_u16 v123, v13
	ds_read_u16 v124, v15
	s_waitcnt lgkmcnt(7)
	v_lshlrev_b32_e32 v17, 16, v2
	v_add_u32_e32 v2, 0x13ce0, v0
	ds_read_u16 v2, v2
	v_readfirstlane_b32 s4, v114
	v_add_f32_e32 v114, 0, v49
	s_waitcnt lgkmcnt(7)
	v_lshlrev_b32_e32 v15, 16, v4
	s_waitcnt lgkmcnt(6)
	v_lshlrev_b32_e32 v13, 16, v6
	s_waitcnt lgkmcnt(5)
	v_lshlrev_b32_e32 v11, 16, v8
	s_waitcnt lgkmcnt(4)
	v_lshlrev_b32_e32 v10, 16, v10
	s_waitcnt lgkmcnt(3)
	v_lshlrev_b32_e32 v8, 16, v122
	s_waitcnt lgkmcnt(2)
	v_lshlrev_b32_e32 v6, 16, v123
	s_waitcnt lgkmcnt(1)
	v_lshlrev_b32_e32 v4, 16, v124
	s_waitcnt lgkmcnt(0)
	v_lshlrev_b32_e32 v2, 16, v2
	s_cselect_b64 s[6:7], -1, 0
	s_mov_b64 s[8:9], -1
	s_cmpk_gt_u32 s4, 0x7f
	v_add_f32_e32 v114, v114, v115
	s_cbranch_scc0 .LBB0_595
	ds_read_u16 v129, v0
	ds_read_u16 v130, v0 offset:1040
	ds_read_u16 v131, v0 offset:2080
	ds_read_u16 v132, v0 offset:3120
	ds_read_u16 v133, v0 offset:4160
	ds_read_u16 v134, v0 offset:5200
	ds_read_u16 v135, v0 offset:6240
	ds_read_u16 v136, v0 offset:7280
	ds_read_u16 v122, v0 offset:12480
	ds_read_u16 v123, v0 offset:13520
	ds_read_u16 v125, v0 offset:8320
	ds_read_u16 v126, v0 offset:9360
	ds_read_u16 v137, v0 offset:10400
	ds_read_u16 v138, v0 offset:11440
	s_waitcnt lgkmcnt(5)
	v_lshlrev_b32_e32 v124, 16, v122
	s_waitcnt lgkmcnt(4)
	v_lshlrev_b32_e32 v122, 16, v123
	s_ashr_i32 s14, s4, 7
	v_add_f32_e32 v123, v114, v122
	v_add_f32_e32 v123, v123, v124
	s_waitcnt lgkmcnt(3)
	v_lshlrev_b32_e32 v128, 16, v125
	s_waitcnt lgkmcnt(2)
	v_lshlrev_b32_e32 v127, 16, v126
	s_waitcnt lgkmcnt(1)
	v_lshlrev_b32_e32 v126, 16, v137
	s_waitcnt lgkmcnt(0)
	v_lshlrev_b32_e32 v125, 16, v138
	s_mov_b64 s[12:13], -1
	s_mov_b64 s[8:9], 0
	s_cmp_lt_i32 s14, 2
	s_mov_b64 s[10:11], 0
	s_cbranch_scc1 .LBB0_590
	s_cmp_eq_u32 s14, 2
	s_mov_b64 s[10:11], -1
	s_cbranch_scc0 .LBB0_587
	v_add_f32_e32 v137, v123, v125
	v_add_f32_e32 v137, v137, v126
	v_add_f32_e32 v137, v137, v127
	v_mov_b32_e32 v139, 0x3e000000
	v_add_f32_e32 v137, v137, v128
	v_cndmask_b32_e64 v138, v139, 1.0, s[6:7]
	v_fma_f32 v137, v138, v137, -v49
	v_cvt_pk_bf16_f32 v137, v137, s0
	ds_write_b16 v0, v137
	v_add_f32_e32 v137, v46, v49
	v_add_f32_e32 v137, v137, v115
	v_add_f32_e32 v137, v137, v122
	v_add_f32_e32 v137, v137, v124
	v_add_f32_e32 v137, v137, v125
	v_add_f32_e32 v137, v137, v126
	v_add_f32_e32 v137, v137, v127
	v_cndmask_b32_e64 v138, v139, 0.5, s[6:7]
	v_fma_f32 v137, v138, v137, -v46
	v_cvt_pk_bf16_f32 v137, v137, s0
	ds_write_b16 v0, v137 offset:1040
	v_add_f32_e32 v137, v43, v46
	v_add_f32_e32 v137, v137, v49
	v_add_f32_e32 v137, v137, v115
	v_add_f32_e32 v137, v137, v122
	v_add_f32_e32 v137, v137, v124
	v_add_f32_e32 v137, v137, v125
	v_mov_b32_e32 v138, 0x3eaaaaab
	v_add_f32_e32 v137, v137, v126
	v_cndmask_b32_e64 v138, v139, v138, s[6:7]
	v_fma_f32 v137, v138, v137, -v43
	v_cvt_pk_bf16_f32 v137, v137, s0
	ds_write_b16 v0, v137 offset:2080
	v_add_f32_e32 v137, v41, v43
	v_add_f32_e32 v137, v137, v46
	v_add_f32_e32 v137, v137, v49
	v_add_f32_e32 v137, v137, v115
	v_add_f32_e32 v137, v137, v122
	v_add_f32_e32 v137, v137, v124
	v_mov_b32_e32 v138, 0x3e800000
	v_add_f32_e32 v137, v137, v125
	v_cndmask_b32_e64 v138, v139, v138, s[6:7]
	v_fma_f32 v137, v138, v137, -v41
	v_cvt_pk_bf16_f32 v137, v137, s0
	ds_write_b16 v0, v137 offset:3120
	v_add_f32_e32 v137, v38, v41
	v_add_f32_e32 v137, v137, v43
	v_add_f32_e32 v137, v137, v46
	v_add_f32_e32 v137, v137, v49
	v_add_f32_e32 v137, v137, v115
	v_add_f32_e32 v137, v137, v122
	v_mov_b32_e32 v138, 0x3e4ccccd
	v_add_f32_e32 v137, v137, v124
	v_cndmask_b32_e64 v138, v139, v138, s[6:7]
	v_fma_f32 v137, v138, v137, -v38
	v_cvt_pk_bf16_f32 v137, v137, s0
	ds_write_b16 v0, v137 offset:4160
	v_add_f32_e32 v137, v35, v38
	v_add_f32_e32 v137, v137, v41
	v_add_f32_e32 v137, v137, v43
	v_add_f32_e32 v137, v137, v46
	v_add_f32_e32 v137, v137, v49
	v_add_f32_e32 v137, v137, v115
	v_mov_b32_e32 v138, 0x3e2aaaab
	v_add_f32_e32 v137, v137, v122
	v_cndmask_b32_e64 v138, v139, v138, s[6:7]
	v_fma_f32 v137, v138, v137, -v35
	v_cvt_pk_bf16_f32 v137, v137, s0
	ds_write_b16 v0, v137 offset:5200
	v_add_f32_e32 v137, v32, v35
	v_add_f32_e32 v137, v137, v38
	v_add_f32_e32 v137, v137, v41
	v_add_f32_e32 v137, v137, v43
	v_add_f32_e32 v137, v137, v46
	v_add_f32_e32 v137, v137, v49
	v_mov_b32_e32 v138, 0x3e124925
	v_add_f32_e32 v137, v137, v115
	v_cndmask_b32_e64 v138, v139, v138, s[6:7]
	v_fma_f32 v137, v138, v137, -v32
	v_cvt_pk_bf16_f32 v137, v137, s0
	ds_write_b16 v0, v137 offset:6240
	v_add_f32_e32 v137, v39, v32
	v_add_f32_e32 v137, v137, v35
	v_add_f32_e32 v137, v137, v38
	v_add_f32_e32 v137, v137, v41
	v_add_f32_e32 v137, v137, v43
	v_add_f32_e32 v137, v137, v46
	v_add_f32_e32 v137, v137, v49
	s_mov_b32 s4, 0x3e000000
	v_fma_f32 v137, v137, s4, -v39
	v_cvt_pk_bf16_f32 v137, v137, s0
	ds_write_b16 v0, v137 offset:7280
	v_add_f32_e32 v137, v36, v39
	v_add_f32_e32 v137, v137, v32
	v_add_f32_e32 v137, v137, v35
	v_add_f32_e32 v137, v137, v38
	v_add_f32_e32 v137, v137, v41
	v_add_f32_e32 v137, v137, v43
	v_add_f32_e32 v137, v137, v46
	v_fma_f32 v137, v137, s4, -v36
	v_cvt_pk_bf16_f32 v137, v137, s0
	ds_write_b16 v0, v137 offset:8320
	v_add_f32_e32 v137, v33, v36
	v_add_f32_e32 v137, v137, v39
	v_add_f32_e32 v137, v137, v32
	v_add_f32_e32 v137, v137, v35
	v_add_f32_e32 v137, v137, v38
	v_add_f32_e32 v137, v137, v41
	v_add_f32_e32 v137, v137, v43
	v_fma_f32 v137, v137, s4, -v33
	v_cvt_pk_bf16_f32 v137, v137, s0
	ds_write_b16 v0, v137 offset:9360
	v_add_f32_e32 v137, v29, v33
	v_add_f32_e32 v137, v137, v36
	v_add_f32_e32 v137, v137, v39
	v_add_f32_e32 v137, v137, v32
	v_add_f32_e32 v137, v137, v35
	v_add_f32_e32 v137, v137, v38
	v_add_f32_e32 v137, v137, v41
	v_fma_f32 v137, v137, s4, -v29
	v_cvt_pk_bf16_f32 v137, v137, s0
	ds_write_b16 v0, v137 offset:10400
	v_add_f32_e32 v137, v26, v29
	v_add_f32_e32 v137, v137, v33
	v_add_f32_e32 v137, v137, v36
	v_add_f32_e32 v137, v137, v39
	v_add_f32_e32 v137, v137, v32
	v_add_f32_e32 v137, v137, v35
	v_add_f32_e32 v137, v137, v38
	v_fma_f32 v137, v137, s4, -v26
	v_cvt_pk_bf16_f32 v137, v137, s0
	ds_write_b16 v0, v137 offset:11440
	v_add_f32_e32 v137, v24, v26
	v_add_f32_e32 v137, v137, v29
	v_add_f32_e32 v137, v137, v33
	v_add_f32_e32 v137, v137, v36
	v_add_f32_e32 v137, v137, v39
	v_add_f32_e32 v137, v137, v32
	v_add_f32_e32 v137, v137, v35
	v_fma_f32 v137, v137, s4, -v24
	v_cvt_pk_bf16_f32 v137, v137, s0
	ds_write_b16 v0, v137 offset:12480
	v_add_f32_e32 v137, v22, v24
	v_add_f32_e32 v137, v137, v26
	v_add_f32_e32 v137, v137, v29
	v_add_f32_e32 v137, v137, v33
	v_add_f32_e32 v137, v137, v36
	v_add_f32_e32 v137, v137, v39
	v_add_f32_e32 v137, v137, v32
	v_fma_f32 v137, v137, s4, -v22
	v_cvt_pk_bf16_f32 v137, v137, s0
	ds_write_b16 v0, v137 offset:13520
	v_add_f32_e32 v137, v20, v22
	v_add_f32_e32 v137, v137, v24
	v_add_f32_e32 v137, v137, v26
	v_add_f32_e32 v137, v137, v29
	v_add_f32_e32 v137, v137, v33
	v_add_f32_e32 v137, v137, v36
	v_add_f32_e32 v137, v137, v39
	v_fma_f32 v137, v137, s4, -v20
	v_cvt_pk_bf16_f32 v137, v137, s0
	ds_write_b16 v0, v137 offset:14560
	v_add_f32_e32 v137, v64, v20
	v_add_f32_e32 v137, v137, v22
	v_add_f32_e32 v137, v137, v24
	v_add_f32_e32 v137, v137, v26
	v_add_f32_e32 v137, v137, v29
	v_add_f32_e32 v137, v137, v33
	v_add_f32_e32 v137, v137, v36
	v_fma_f32 v137, v137, s4, -v64
	v_cvt_pk_bf16_f32 v137, v137, s0
	ds_write_b16 v0, v137 offset:15600
	v_add_f32_e32 v137, v62, v64
	v_add_f32_e32 v137, v137, v20
	v_add_f32_e32 v137, v137, v22
	v_add_f32_e32 v137, v137, v24
	v_add_f32_e32 v137, v137, v26
	v_add_f32_e32 v137, v137, v29
	v_add_f32_e32 v137, v137, v33
	v_fma_f32 v137, v137, s4, -v62
	v_cvt_pk_bf16_f32 v137, v137, s0
	ds_write_b16 v0, v137 offset:16640
	v_add_f32_e32 v137, v65, v62
	v_add_f32_e32 v137, v137, v64
	v_add_f32_e32 v137, v137, v20
	v_add_f32_e32 v137, v137, v22
	v_add_f32_e32 v137, v137, v24
	v_add_f32_e32 v137, v137, v26
	v_add_f32_e32 v137, v137, v29
	v_fma_f32 v137, v137, s4, -v65
	v_cvt_pk_bf16_f32 v137, v137, s0
	ds_write_b16 v0, v137 offset:17680
	v_add_f32_e32 v137, v63, v65
	v_add_f32_e32 v137, v137, v62
	v_add_f32_e32 v137, v137, v64
	v_add_f32_e32 v137, v137, v20
	v_add_f32_e32 v137, v137, v22
	v_add_f32_e32 v137, v137, v24
	v_add_f32_e32 v137, v137, v26
	v_fma_f32 v137, v137, s4, -v63
	v_cvt_pk_bf16_f32 v137, v137, s0
	ds_write_b16 v0, v137 offset:18720
	v_add_f32_e32 v137, v61, v63
	v_add_f32_e32 v137, v137, v65
	v_add_f32_e32 v137, v137, v62
	v_add_f32_e32 v137, v137, v64
	v_add_f32_e32 v137, v137, v20
	v_add_f32_e32 v137, v137, v22
	v_add_f32_e32 v137, v137, v24
	v_fma_f32 v137, v137, s4, -v61
	v_cvt_pk_bf16_f32 v137, v137, s0
	ds_write_b16 v0, v137 offset:19760
	v_add_f32_e32 v137, v60, v61
	v_add_f32_e32 v137, v137, v63
	v_add_f32_e32 v137, v137, v65
	v_add_f32_e32 v137, v137, v62
	v_add_f32_e32 v137, v137, v64
	v_add_f32_e32 v137, v137, v20
	v_add_f32_e32 v137, v137, v22
	v_fma_f32 v137, v137, s4, -v60
	v_cvt_pk_bf16_f32 v137, v137, s0
	ds_write_b16 v0, v137 offset:20800
	v_add_f32_e32 v137, v59, v60
	v_add_f32_e32 v137, v137, v61
	v_add_f32_e32 v137, v137, v63
	v_add_f32_e32 v137, v137, v65
	v_add_f32_e32 v137, v137, v62
	v_add_f32_e32 v137, v137, v64
	v_add_f32_e32 v137, v137, v20
	v_fma_f32 v137, v137, s4, -v59
	v_cvt_pk_bf16_f32 v137, v137, s0
	ds_write_b16 v0, v137 offset:21840
	v_add_f32_e32 v137, v58, v59
	v_add_f32_e32 v137, v137, v60
	v_add_f32_e32 v137, v137, v61
	v_add_f32_e32 v137, v137, v63
	v_add_f32_e32 v137, v137, v65
	v_add_f32_e32 v137, v137, v62
	v_add_f32_e32 v137, v137, v64
	v_fma_f32 v137, v137, s4, -v58
	v_cvt_pk_bf16_f32 v137, v137, s0
	ds_write_b16 v0, v137 offset:22880
	v_add_f32_e32 v137, v56, v58
	v_add_f32_e32 v137, v137, v59
	v_add_f32_e32 v137, v137, v60
	v_add_f32_e32 v137, v137, v61
	v_add_f32_e32 v137, v137, v63
	v_add_f32_e32 v137, v137, v65
	v_add_f32_e32 v137, v137, v62
	v_fma_f32 v137, v137, s4, -v56
	v_cvt_pk_bf16_f32 v137, v137, s0
	ds_write_b16 v0, v137 offset:23920
	v_add_f32_e32 v137, v54, v56
	v_add_f32_e32 v137, v137, v58
	v_add_f32_e32 v137, v137, v59
	v_add_f32_e32 v137, v137, v60
	v_add_f32_e32 v137, v137, v61
	v_add_f32_e32 v137, v137, v63
	v_add_f32_e32 v137, v137, v65
	v_fma_f32 v137, v137, s4, -v54
	v_cvt_pk_bf16_f32 v137, v137, s0
	ds_write_b16 v0, v137 offset:24960
	v_add_f32_e32 v137, v57, v54
	v_add_f32_e32 v137, v137, v56
	v_add_f32_e32 v137, v137, v58
	v_add_f32_e32 v137, v137, v59
	v_add_f32_e32 v137, v137, v60
	v_add_f32_e32 v137, v137, v61
	v_add_f32_e32 v137, v137, v63
	v_fma_f32 v137, v137, s4, -v57
	v_cvt_pk_bf16_f32 v137, v137, s0
	ds_write_b16 v0, v137 offset:26000
	v_add_f32_e32 v137, v55, v57
	v_add_f32_e32 v137, v137, v54
	v_add_f32_e32 v137, v137, v56
	v_add_f32_e32 v137, v137, v58
	v_add_f32_e32 v137, v137, v59
	v_add_f32_e32 v137, v137, v60
	v_add_f32_e32 v137, v137, v61
	v_fma_f32 v137, v137, s4, -v55
	v_cvt_pk_bf16_f32 v137, v137, s0
	ds_write_b16 v0, v137 offset:27040
	v_add_f32_e32 v137, v53, v55
	v_add_f32_e32 v137, v137, v57
	v_add_f32_e32 v137, v137, v54
	v_add_f32_e32 v137, v137, v56
	v_add_f32_e32 v137, v137, v58
	v_add_f32_e32 v137, v137, v59
	v_add_f32_e32 v137, v137, v60
	v_fma_f32 v137, v137, s4, -v53
	v_cvt_pk_bf16_f32 v137, v137, s0
	ds_write_b16 v0, v137 offset:28080
	v_add_f32_e32 v137, v52, v53
	v_add_f32_e32 v137, v137, v55
	v_add_f32_e32 v137, v137, v57
	v_add_f32_e32 v137, v137, v54
	v_add_f32_e32 v137, v137, v56
	v_add_f32_e32 v137, v137, v58
	v_add_f32_e32 v137, v137, v59
	v_fma_f32 v137, v137, s4, -v52
	v_cvt_pk_bf16_f32 v137, v137, s0
	ds_write_b16 v0, v137 offset:29120
	v_add_f32_e32 v137, v51, v52
	v_add_f32_e32 v137, v137, v53
	v_add_f32_e32 v137, v137, v55
	v_add_f32_e32 v137, v137, v57
	v_add_f32_e32 v137, v137, v54
	v_add_f32_e32 v137, v137, v56
	v_add_f32_e32 v137, v137, v58
	v_fma_f32 v137, v137, s4, -v51
	v_cvt_pk_bf16_f32 v137, v137, s0
	ds_write_b16 v0, v137 offset:30160
	v_add_f32_e32 v137, v50, v51
	v_add_f32_e32 v137, v137, v52
	v_add_f32_e32 v137, v137, v53
	v_add_f32_e32 v137, v137, v55
	v_add_f32_e32 v137, v137, v57
	v_add_f32_e32 v137, v137, v54
	v_add_f32_e32 v137, v137, v56
	v_fma_f32 v137, v137, s4, -v50
	v_cvt_pk_bf16_f32 v137, v137, s0
	ds_write_b16 v0, v137 offset:31200
	v_add_f32_e32 v137, v47, v50
	v_add_f32_e32 v137, v137, v51
	v_add_f32_e32 v137, v137, v52
	v_add_f32_e32 v137, v137, v53
	v_add_f32_e32 v137, v137, v55
	v_add_f32_e32 v137, v137, v57
	v_add_f32_e32 v137, v137, v54
	v_fma_f32 v137, v137, s4, -v47
	v_cvt_pk_bf16_f32 v137, v137, s0
	ds_write_b16 v0, v137 offset:32240
	v_add_f32_e32 v137, v44, v47
	v_add_f32_e32 v137, v137, v50
	v_add_f32_e32 v137, v137, v51
	v_add_f32_e32 v137, v137, v52
	v_add_f32_e32 v137, v137, v53
	v_add_f32_e32 v137, v137, v55
	v_add_f32_e32 v137, v137, v57
	v_fma_f32 v137, v137, s4, -v44
	v_cvt_pk_bf16_f32 v137, v137, s0
	ds_write_b16 v0, v137 offset:33280
	v_add_f32_e32 v137, v48, v44
	v_add_f32_e32 v137, v137, v47
	v_add_f32_e32 v137, v137, v50
	v_add_f32_e32 v137, v137, v51
	v_add_f32_e32 v137, v137, v52
	v_add_f32_e32 v137, v137, v53
	v_add_f32_e32 v137, v137, v55
	v_fma_f32 v137, v137, s4, -v48
	v_cvt_pk_bf16_f32 v137, v137, s0
	ds_write_b16 v0, v137 offset:34320
	v_add_f32_e32 v137, v45, v48
	v_add_f32_e32 v137, v137, v44
	v_add_f32_e32 v137, v137, v47
	v_add_f32_e32 v137, v137, v50
	v_add_f32_e32 v137, v137, v51
	v_add_f32_e32 v137, v137, v52
	v_add_f32_e32 v137, v137, v53
	v_fma_f32 v137, v137, s4, -v45
	v_cvt_pk_bf16_f32 v137, v137, s0
	ds_write_b16 v0, v137 offset:35360
	v_add_f32_e32 v137, v42, v45
	v_add_f32_e32 v137, v137, v48
	v_add_f32_e32 v137, v137, v44
	v_add_f32_e32 v137, v137, v47
	v_add_f32_e32 v137, v137, v50
	v_add_f32_e32 v137, v137, v51
	v_add_f32_e32 v137, v137, v52
	v_fma_f32 v137, v137, s4, -v42
	v_cvt_pk_bf16_f32 v137, v137, s0
	ds_write_b16 v0, v137 offset:36400
	v_add_f32_e32 v137, v40, v42
	v_add_f32_e32 v137, v137, v45
	v_add_f32_e32 v137, v137, v48
	v_add_f32_e32 v137, v137, v44
	v_add_f32_e32 v137, v137, v47
	v_add_f32_e32 v137, v137, v50
	v_add_f32_e32 v137, v137, v51
	v_fma_f32 v137, v137, s4, -v40
	v_cvt_pk_bf16_f32 v137, v137, s0
	ds_write_b16 v0, v137 offset:37440
	v_add_f32_e32 v137, v37, v40
	v_add_f32_e32 v137, v137, v42
	v_add_f32_e32 v137, v137, v45
	v_add_f32_e32 v137, v137, v48
	v_add_f32_e32 v137, v137, v44
	v_add_f32_e32 v137, v137, v47
	v_add_f32_e32 v137, v137, v50
	v_fma_f32 v137, v137, s4, -v37
	v_cvt_pk_bf16_f32 v137, v137, s0
	ds_write_b16 v0, v137 offset:38480
	v_add_f32_e32 v137, v34, v37
	v_add_f32_e32 v137, v137, v40
	v_add_f32_e32 v137, v137, v42
	v_add_f32_e32 v137, v137, v45
	v_add_f32_e32 v137, v137, v48
	v_add_f32_e32 v137, v137, v44
	v_add_f32_e32 v137, v137, v47
	v_fma_f32 v137, v137, s4, -v34
	v_cvt_pk_bf16_f32 v137, v137, s0
	ds_write_b16 v0, v137 offset:39520
	v_add_f32_e32 v137, v30, v34
	v_add_f32_e32 v137, v137, v37
	v_add_f32_e32 v137, v137, v40
	v_add_f32_e32 v137, v137, v42
	v_add_f32_e32 v137, v137, v45
	v_add_f32_e32 v137, v137, v48
	v_add_f32_e32 v137, v137, v44
	v_fma_f32 v137, v137, s4, -v30
	v_cvt_pk_bf16_f32 v137, v137, s0
	ds_write_b16 v0, v137 offset:40560
	v_add_f32_e32 v137, v27, v30
	v_add_f32_e32 v137, v137, v34
	v_add_f32_e32 v137, v137, v37
	v_add_f32_e32 v137, v137, v40
	v_add_f32_e32 v137, v137, v42
	v_add_f32_e32 v137, v137, v45
	v_add_f32_e32 v137, v137, v48
	v_fma_f32 v137, v137, s4, -v27
	v_cvt_pk_bf16_f32 v137, v137, s0
	ds_write_b16 v0, v137 offset:41600
	v_add_f32_e32 v137, v31, v27
	v_add_f32_e32 v137, v137, v30
	v_add_f32_e32 v137, v137, v34
	v_add_f32_e32 v137, v137, v37
	v_add_f32_e32 v137, v137, v40
	v_add_f32_e32 v137, v137, v42
	v_add_f32_e32 v137, v137, v45
	v_fma_f32 v137, v137, s4, -v31
	v_cvt_pk_bf16_f32 v137, v137, s0
	ds_write_b16 v0, v137 offset:42640
	v_add_f32_e32 v137, v28, v31
	v_add_f32_e32 v137, v137, v27
	v_add_f32_e32 v137, v137, v30
	v_add_f32_e32 v137, v137, v34
	v_add_f32_e32 v137, v137, v37
	v_add_f32_e32 v137, v137, v40
	v_add_f32_e32 v137, v137, v42
	v_fma_f32 v137, v137, s4, -v28
	v_cvt_pk_bf16_f32 v137, v137, s0
	ds_write_b16 v0, v137 offset:43680
	v_add_f32_e32 v137, v25, v28
	v_add_f32_e32 v137, v137, v31
	v_add_f32_e32 v137, v137, v27
	v_add_f32_e32 v137, v137, v30
	v_add_f32_e32 v137, v137, v34
	v_add_f32_e32 v137, v137, v37
	v_add_f32_e32 v137, v137, v40
	v_fma_f32 v137, v137, s4, -v25
	v_cvt_pk_bf16_f32 v137, v137, s0
	ds_write_b16 v0, v137 offset:44720
	v_add_f32_e32 v137, v23, v25
	v_add_f32_e32 v137, v137, v28
	v_add_f32_e32 v137, v137, v31
	v_add_f32_e32 v137, v137, v27
	v_add_f32_e32 v137, v137, v30
	v_add_f32_e32 v137, v137, v34
	v_add_f32_e32 v137, v137, v37
	v_fma_f32 v137, v137, s4, -v23
	v_cvt_pk_bf16_f32 v137, v137, s0
	ds_write_b16 v0, v137 offset:45760
	v_add_f32_e32 v137, v21, v23
	v_add_f32_e32 v137, v137, v25
	v_add_f32_e32 v137, v137, v28
	v_add_f32_e32 v137, v137, v31
	v_add_f32_e32 v137, v137, v27
	v_add_f32_e32 v137, v137, v30
	v_add_f32_e32 v137, v137, v34
	v_fma_f32 v137, v137, s4, -v21
	v_cvt_pk_bf16_f32 v137, v137, s0
	ds_write_b16 v0, v137 offset:46800
	v_add_f32_e32 v137, v19, v21
	v_add_f32_e32 v137, v137, v23
	v_add_f32_e32 v137, v137, v25
	v_add_f32_e32 v137, v137, v28
	v_add_f32_e32 v137, v137, v31
	v_add_f32_e32 v137, v137, v27
	v_add_f32_e32 v137, v137, v30
	v_fma_f32 v137, v137, s4, -v19
	v_cvt_pk_bf16_f32 v137, v137, s0
	ds_write_b16 v0, v137 offset:47840
	v_add_f32_e32 v137, v18, v19
	v_add_f32_e32 v137, v137, v21
	v_add_f32_e32 v137, v137, v23
	v_add_f32_e32 v137, v137, v25
	v_add_f32_e32 v137, v137, v28
	v_add_f32_e32 v137, v137, v31
	v_add_f32_e32 v137, v137, v27
	v_fma_f32 v137, v137, s4, -v18
	v_cvt_pk_bf16_f32 v137, v137, s0
	ds_write_b16 v0, v137 offset:48880
	v_add_f32_e32 v137, v16, v18
	v_add_f32_e32 v137, v137, v19
	v_add_f32_e32 v137, v137, v21
	v_add_f32_e32 v137, v137, v23
	v_add_f32_e32 v137, v137, v25
	v_add_f32_e32 v137, v137, v28
	v_add_f32_e32 v137, v137, v31
	v_fma_f32 v137, v137, s4, -v16
	v_cvt_pk_bf16_f32 v137, v137, s0
	ds_write_b16 v0, v137 offset:49920
	v_add_f32_e32 v137, v14, v16
	v_add_f32_e32 v137, v137, v18
	v_add_f32_e32 v137, v137, v19
	v_add_f32_e32 v137, v137, v21
	v_add_f32_e32 v137, v137, v23
	v_add_f32_e32 v137, v137, v25
	v_add_f32_e32 v137, v137, v28
	v_fma_f32 v137, v137, s4, -v14
	v_cvt_pk_bf16_f32 v137, v137, s0
	ds_write_b16 v0, v137 offset:50960
	v_add_f32_e32 v137, v12, v14
	v_add_f32_e32 v137, v137, v16
	v_add_f32_e32 v137, v137, v18
	v_add_f32_e32 v137, v137, v19
	v_add_f32_e32 v137, v137, v21
	v_add_f32_e32 v137, v137, v23
	v_add_f32_e32 v137, v137, v25
	v_fma_f32 v137, v137, s4, -v12
	v_cvt_pk_bf16_f32 v137, v137, s0
	ds_write_b16 v0, v137 offset:52000
	v_add_f32_e32 v137, v9, v12
	v_add_f32_e32 v137, v137, v14
	v_add_f32_e32 v137, v137, v16
	v_add_f32_e32 v137, v137, v18
	v_add_f32_e32 v137, v137, v19
	v_add_f32_e32 v137, v137, v21
	v_add_f32_e32 v137, v137, v23
	v_fma_f32 v137, v137, s4, -v9
	v_cvt_pk_bf16_f32 v137, v137, s0
	ds_write_b16 v0, v137 offset:53040
	v_add_f32_e32 v137, v7, v9
	v_add_f32_e32 v137, v137, v12
	v_add_f32_e32 v137, v137, v14
	v_add_f32_e32 v137, v137, v16
	v_add_f32_e32 v137, v137, v18
	v_add_f32_e32 v137, v137, v19
	v_add_f32_e32 v137, v137, v21
	v_fma_f32 v137, v137, s4, -v7
	v_cvt_pk_bf16_f32 v137, v137, s0
	ds_write_b16 v0, v137 offset:54080
	v_add_f32_e32 v137, v5, v7
	v_add_f32_e32 v137, v137, v9
	v_add_f32_e32 v137, v137, v12
	v_add_f32_e32 v137, v137, v14
	v_add_f32_e32 v137, v137, v16
	v_add_f32_e32 v137, v137, v18
	v_add_f32_e32 v137, v137, v19
	v_fma_f32 v137, v137, s4, -v5
	v_cvt_pk_bf16_f32 v137, v137, s0
	ds_write_b16 v0, v137 offset:55120
	v_add_f32_e32 v137, v3, v5
	v_add_f32_e32 v137, v137, v7
	v_add_f32_e32 v137, v137, v9
	v_add_f32_e32 v137, v137, v12
	v_add_f32_e32 v137, v137, v14
	v_add_f32_e32 v137, v137, v16
	v_add_f32_e32 v137, v137, v18
	v_fma_f32 v137, v137, s4, -v3
	v_cvt_pk_bf16_f32 v137, v137, s0
	ds_write_b16 v0, v137 offset:56160
	v_add_f32_e32 v137, v17, v3
	v_add_f32_e32 v137, v137, v5
	v_add_f32_e32 v137, v137, v7
	v_add_f32_e32 v137, v137, v9
	v_add_f32_e32 v137, v137, v12
	v_add_f32_e32 v137, v137, v14
	v_add_f32_e32 v137, v137, v16
	v_fma_f32 v137, v137, s4, -v17
	v_cvt_pk_bf16_f32 v137, v137, s0
	ds_write_b16 v0, v137 offset:57200
	v_add_f32_e32 v137, v15, v17
	v_add_f32_e32 v137, v137, v3
	v_add_f32_e32 v137, v137, v5
	v_add_f32_e32 v137, v137, v7
	v_add_f32_e32 v137, v137, v9
	v_add_f32_e32 v137, v137, v12
	v_add_f32_e32 v137, v137, v14
	v_fma_f32 v137, v137, s4, -v15
	v_cvt_pk_bf16_f32 v137, v137, s0
	ds_write_b16 v0, v137 offset:58240
	v_add_f32_e32 v137, v13, v15
	v_add_f32_e32 v137, v137, v17
	v_add_f32_e32 v137, v137, v3
	v_add_f32_e32 v137, v137, v5
	v_add_f32_e32 v137, v137, v7
	v_add_f32_e32 v137, v137, v9
	v_add_f32_e32 v137, v137, v12
	v_fma_f32 v137, v137, s4, -v13
	v_cvt_pk_bf16_f32 v137, v137, s0
	ds_write_b16 v0, v137 offset:59280
	v_add_f32_e32 v137, v11, v13
	v_add_f32_e32 v137, v137, v15
	v_add_f32_e32 v137, v137, v17
	v_add_f32_e32 v137, v137, v3
	v_add_f32_e32 v137, v137, v5
	v_add_f32_e32 v137, v137, v7
	v_add_f32_e32 v137, v137, v9
	v_fma_f32 v137, v137, s4, -v11
	v_cvt_pk_bf16_f32 v137, v137, s0
	ds_write_b16 v0, v137 offset:60320
	v_add_f32_e32 v137, v10, v11
	v_add_f32_e32 v137, v137, v13
	v_add_f32_e32 v137, v137, v15
	v_add_f32_e32 v137, v137, v17
	v_add_f32_e32 v137, v137, v3
	v_add_f32_e32 v137, v137, v5
	v_add_f32_e32 v137, v137, v7
	v_fma_f32 v137, v137, s4, -v10
	v_cvt_pk_bf16_f32 v137, v137, s0
	ds_write_b16 v0, v137 offset:61360
	v_add_f32_e32 v137, v8, v10
	v_add_f32_e32 v137, v137, v11
	v_add_f32_e32 v137, v137, v13
	v_add_f32_e32 v137, v137, v15
	v_add_f32_e32 v137, v137, v17
	v_add_f32_e32 v137, v137, v3
	v_add_f32_e32 v137, v137, v5
	v_fma_f32 v137, v137, s4, -v8
	v_cvt_pk_bf16_f32 v137, v137, s0
	ds_write_b16 v0, v137 offset:62400
	v_add_f32_e32 v137, v6, v8
	v_add_f32_e32 v137, v137, v10
	v_add_f32_e32 v137, v137, v11
	v_add_f32_e32 v137, v137, v13
	v_add_f32_e32 v137, v137, v15
	v_add_f32_e32 v137, v137, v17
	v_add_f32_e32 v137, v137, v3
	v_fma_f32 v137, v137, s4, -v6
	v_cvt_pk_bf16_f32 v137, v137, s0
	ds_write_b16 v0, v137 offset:63440
	v_add_f32_e32 v137, v4, v6
	v_add_f32_e32 v137, v137, v8
	v_add_f32_e32 v137, v137, v10
	v_add_f32_e32 v137, v137, v11
	v_add_f32_e32 v137, v137, v13
	v_add_f32_e32 v137, v137, v15
	v_add_f32_e32 v137, v137, v17
	v_fma_f32 v137, v137, s4, -v4
	v_cvt_pk_bf16_f32 v137, v137, s0
	ds_write_b16 v0, v137 offset:64480
	v_add_f32_e32 v137, v2, v4
	v_add_f32_e32 v137, v137, v6
	v_add_f32_e32 v137, v137, v8
	v_add_f32_e32 v137, v137, v10
	v_add_f32_e32 v137, v137, v11
	v_add_f32_e32 v137, v137, v13
	v_add_f32_e32 v137, v137, v15
	v_mul_f32_e32 v137, 0x3e000000, v137
	s_mov_b64 s[10:11], 0

.LBB0_589:
	v_add_f32_e32 v137, v123, v125
	v_add_f32_e32 v137, v137, v126
	v_add_f32_e32 v137, v137, v127
	v_lshlrev_b32_e32 v136, 16, v136
	v_add_f32_e32 v137, v137, v128
	v_lshlrev_b32_e32 v135, 16, v135
	v_add_f32_e32 v137, v137, v136
	v_lshlrev_b32_e32 v134, 16, v134
	v_add_f32_e32 v137, v137, v135
	v_lshlrev_b32_e32 v133, 16, v133
	v_add_f32_e32 v137, v137, v134
	v_lshlrev_b32_e32 v132, 16, v132
	v_add_f32_e32 v137, v137, v133
	v_lshlrev_b32_e32 v131, 16, v131
	v_add_f32_e32 v137, v137, v132
	v_lshlrev_b32_e32 v130, 16, v130
	v_add_f32_e32 v137, v137, v131
	v_lshlrev_b32_e32 v129, 16, v129
	v_add_f32_e32 v137, v137, v130
	v_mov_b32_e32 v138, 0x3d800000
	v_add_f32_e32 v129, v137, v129
	v_cndmask_b32_e64 v137, v138, 1.0, s[6:7]
	v_fma_f32 v129, v137, v129, -v49
	v_cvt_pk_bf16_f32 v129, v129, s0
	ds_write_b16 v0, v129
	v_add_f32_e32 v129, v46, v49
	v_add_f32_e32 v129, v129, v115
	v_add_f32_e32 v129, v129, v122
	v_add_f32_e32 v129, v129, v124
	v_add_f32_e32 v129, v129, v125
	v_add_f32_e32 v129, v129, v126
	v_add_f32_e32 v129, v129, v127
	v_add_f32_e32 v129, v129, v128
	v_add_f32_e32 v129, v129, v136
	v_add_f32_e32 v129, v129, v135
	v_add_f32_e32 v129, v129, v134
	v_add_f32_e32 v129, v129, v133
	v_add_f32_e32 v129, v129, v132
	v_add_f32_e32 v129, v129, v131
	v_add_f32_e32 v129, v129, v130
	v_cndmask_b32_e64 v130, v138, 0.5, s[6:7]
	v_fma_f32 v129, v130, v129, -v46
	v_cvt_pk_bf16_f32 v129, v129, s0
	ds_write_b16 v0, v129 offset:1040
	v_add_f32_e32 v129, v43, v46
	v_add_f32_e32 v129, v129, v49
	v_add_f32_e32 v129, v129, v115
	v_add_f32_e32 v129, v129, v122
	v_add_f32_e32 v129, v129, v124
	v_add_f32_e32 v129, v129, v125
	v_add_f32_e32 v129, v129, v126
	v_add_f32_e32 v129, v129, v127
	v_add_f32_e32 v129, v129, v128
	v_add_f32_e32 v129, v129, v136
	v_add_f32_e32 v129, v129, v135
	v_add_f32_e32 v129, v129, v134
	v_add_f32_e32 v129, v129, v133
	v_add_f32_e32 v129, v129, v132
	v_mov_b32_e32 v130, 0x3eaaaaab
	v_add_f32_e32 v129, v129, v131
	v_cndmask_b32_e64 v130, v138, v130, s[6:7]
	v_fma_f32 v129, v130, v129, -v43
	v_cvt_pk_bf16_f32 v129, v129, s0
	ds_write_b16 v0, v129 offset:2080
	v_add_f32_e32 v129, v41, v43
	v_add_f32_e32 v129, v129, v46
	v_add_f32_e32 v129, v129, v49
	v_add_f32_e32 v129, v129, v115
	v_add_f32_e32 v129, v129, v122
	v_add_f32_e32 v129, v129, v124
	v_add_f32_e32 v129, v129, v125
	v_add_f32_e32 v129, v129, v126
	v_add_f32_e32 v129, v129, v127
	v_add_f32_e32 v129, v129, v128
	v_add_f32_e32 v129, v129, v136
	v_add_f32_e32 v129, v129, v135
	v_add_f32_e32 v129, v129, v134
	v_add_f32_e32 v129, v129, v133
	v_mov_b32_e32 v130, 0x3e800000
	v_add_f32_e32 v129, v129, v132
	v_cndmask_b32_e64 v130, v138, v130, s[6:7]
	v_fma_f32 v129, v130, v129, -v41
	v_cvt_pk_bf16_f32 v129, v129, s0
	ds_write_b16 v0, v129 offset:3120
	v_add_f32_e32 v129, v38, v41
	v_add_f32_e32 v129, v129, v43
	v_add_f32_e32 v129, v129, v46
	v_add_f32_e32 v129, v129, v49
	v_add_f32_e32 v129, v129, v115
	v_add_f32_e32 v129, v129, v122
	v_add_f32_e32 v129, v129, v124
	v_add_f32_e32 v129, v129, v125
	v_add_f32_e32 v129, v129, v126
	v_add_f32_e32 v129, v129, v127
	v_add_f32_e32 v129, v129, v128
	v_add_f32_e32 v129, v129, v136
	v_add_f32_e32 v129, v129, v135
	v_add_f32_e32 v129, v129, v134
	v_mov_b32_e32 v130, 0x3e4ccccd
	v_add_f32_e32 v129, v129, v133
	v_cndmask_b32_e64 v130, v138, v130, s[6:7]
	v_fma_f32 v129, v130, v129, -v38
	v_cvt_pk_bf16_f32 v129, v129, s0
	ds_write_b16 v0, v129 offset:4160
	v_add_f32_e32 v129, v35, v38
	v_add_f32_e32 v129, v129, v41
	v_add_f32_e32 v129, v129, v43
	v_add_f32_e32 v129, v129, v46
	v_add_f32_e32 v129, v129, v49
	v_add_f32_e32 v129, v129, v115
	v_add_f32_e32 v129, v129, v122
	v_add_f32_e32 v129, v129, v124
	v_add_f32_e32 v129, v129, v125
	v_add_f32_e32 v129, v129, v126
	v_add_f32_e32 v129, v129, v127
	v_add_f32_e32 v129, v129, v128
	v_add_f32_e32 v129, v129, v136
	v_add_f32_e32 v129, v129, v135
	v_mov_b32_e32 v130, 0x3e2aaaab
	v_add_f32_e32 v129, v129, v134
	v_cndmask_b32_e64 v130, v138, v130, s[6:7]
	v_fma_f32 v129, v130, v129, -v35
	v_cvt_pk_bf16_f32 v129, v129, s0
	ds_write_b16 v0, v129 offset:5200
	v_add_f32_e32 v129, v32, v35
	v_add_f32_e32 v129, v129, v38
	v_add_f32_e32 v129, v129, v41
	v_add_f32_e32 v129, v129, v43
	v_add_f32_e32 v129, v129, v46
	v_add_f32_e32 v129, v129, v49
	v_add_f32_e32 v129, v129, v115
	v_add_f32_e32 v129, v129, v122
	v_add_f32_e32 v129, v129, v124
	v_add_f32_e32 v129, v129, v125
	v_add_f32_e32 v129, v129, v126
	v_add_f32_e32 v129, v129, v127
	v_add_f32_e32 v129, v129, v128
	v_add_f32_e32 v129, v129, v136
	v_mov_b32_e32 v130, 0x3e124925
	v_add_f32_e32 v129, v129, v135
	v_cndmask_b32_e64 v130, v138, v130, s[6:7]
	v_fma_f32 v129, v130, v129, -v32
	v_cvt_pk_bf16_f32 v129, v129, s0
	ds_write_b16 v0, v129 offset:6240
	v_add_f32_e32 v129, v39, v32
	v_add_f32_e32 v129, v129, v35
	v_add_f32_e32 v129, v129, v38
	v_add_f32_e32 v129, v129, v41
	v_add_f32_e32 v129, v129, v43
	v_add_f32_e32 v129, v129, v46
	v_add_f32_e32 v129, v129, v49
	v_add_f32_e32 v129, v129, v115
	v_add_f32_e32 v129, v129, v122
	v_add_f32_e32 v129, v129, v124
	v_add_f32_e32 v129, v129, v125
	v_add_f32_e32 v129, v129, v126
	v_add_f32_e32 v129, v129, v127
	v_add_f32_e32 v129, v129, v128
	v_mov_b32_e32 v130, 0x3e000000
	v_add_f32_e32 v129, v129, v136
	v_cndmask_b32_e64 v130, v138, v130, s[6:7]
	v_fma_f32 v129, v130, v129, -v39
	v_cvt_pk_bf16_f32 v129, v129, s0
	ds_write_b16 v0, v129 offset:7280
	v_add_f32_e32 v129, v36, v39
	v_add_f32_e32 v129, v129, v32
	v_add_f32_e32 v129, v129, v35
	v_add_f32_e32 v129, v129, v38
	v_add_f32_e32 v129, v129, v41
	v_add_f32_e32 v129, v129, v43
	v_add_f32_e32 v129, v129, v46
	v_add_f32_e32 v129, v129, v49
	v_add_f32_e32 v129, v129, v115
	v_add_f32_e32 v129, v129, v122
	v_add_f32_e32 v129, v129, v124
	v_add_f32_e32 v129, v129, v125
	v_add_f32_e32 v129, v129, v126
	v_add_f32_e32 v129, v129, v127
	v_add_f32_e32 v128, v129, v128
	v_mov_b32_e32 v129, 0x3de38e39
	v_cndmask_b32_e64 v129, v138, v129, s[6:7]
	v_fma_f32 v128, v129, v128, -v36
	v_cvt_pk_bf16_f32 v128, v128, s0
	ds_write_b16 v0, v128 offset:8320
	v_add_f32_e32 v128, v33, v36
	v_add_f32_e32 v128, v128, v39
	v_add_f32_e32 v128, v128, v32
	v_add_f32_e32 v128, v128, v35
	v_add_f32_e32 v128, v128, v38
	v_add_f32_e32 v128, v128, v41
	v_add_f32_e32 v128, v128, v43
	v_add_f32_e32 v128, v128, v46
	v_add_f32_e32 v128, v128, v49
	v_add_f32_e32 v128, v128, v115
	v_add_f32_e32 v128, v128, v122
	v_add_f32_e32 v128, v128, v124
	v_add_f32_e32 v128, v128, v125
	v_add_f32_e32 v128, v128, v126
	v_add_f32_e32 v127, v128, v127
	v_mov_b32_e32 v128, 0x3dcccccd
	v_cndmask_b32_e64 v128, v138, v128, s[6:7]
	v_fma_f32 v127, v128, v127, -v33
	v_cvt_pk_bf16_f32 v127, v127, s0
	ds_write_b16 v0, v127 offset:9360
	v_add_f32_e32 v127, v29, v33
	v_add_f32_e32 v127, v127, v36
	v_add_f32_e32 v127, v127, v39
	v_add_f32_e32 v127, v127, v32
	v_add_f32_e32 v127, v127, v35
	v_add_f32_e32 v127, v127, v38
	v_add_f32_e32 v127, v127, v41
	v_add_f32_e32 v127, v127, v43
	v_add_f32_e32 v127, v127, v46
	v_add_f32_e32 v127, v127, v49
	v_add_f32_e32 v127, v127, v115
	v_add_f32_e32 v127, v127, v122
	v_add_f32_e32 v127, v127, v124
	v_add_f32_e32 v127, v127, v125
	v_add_f32_e32 v126, v127, v126
	v_mov_b32_e32 v127, 0x3dba2e8c
	v_cndmask_b32_e64 v127, v138, v127, s[6:7]
	v_fma_f32 v126, v127, v126, -v29
	v_cvt_pk_bf16_f32 v126, v126, s0
	ds_write_b16 v0, v126 offset:10400
	v_add_f32_e32 v126, v26, v29
	v_add_f32_e32 v126, v126, v33
	v_add_f32_e32 v126, v126, v36
	v_add_f32_e32 v126, v126, v39
	v_add_f32_e32 v126, v126, v32
	v_add_f32_e32 v126, v126, v35
	v_add_f32_e32 v126, v126, v38
	v_add_f32_e32 v126, v126, v41
	v_add_f32_e32 v126, v126, v43
	v_add_f32_e32 v126, v126, v46
	v_add_f32_e32 v126, v126, v49
	v_add_f32_e32 v126, v126, v115
	v_add_f32_e32 v126, v126, v122
	v_add_f32_e32 v126, v126, v124
	v_add_f32_e32 v125, v126, v125
	v_mov_b32_e32 v126, 0x3daaaaab
	v_cndmask_b32_e64 v126, v138, v126, s[6:7]
	v_fma_f32 v125, v126, v125, -v26
	v_cvt_pk_bf16_f32 v125, v125, s0
	ds_write_b16 v0, v125 offset:11440
	v_add_f32_e32 v125, v24, v26
	v_add_f32_e32 v125, v125, v29
	v_add_f32_e32 v125, v125, v33
	v_add_f32_e32 v125, v125, v36
	v_add_f32_e32 v125, v125, v39
	v_add_f32_e32 v125, v125, v32
	v_add_f32_e32 v125, v125, v35
	v_add_f32_e32 v125, v125, v38
	v_add_f32_e32 v125, v125, v41
	v_add_f32_e32 v125, v125, v43
	v_add_f32_e32 v125, v125, v46
	v_add_f32_e32 v125, v125, v49
	v_add_f32_e32 v125, v125, v115
	v_add_f32_e32 v125, v125, v122
	v_add_f32_e32 v124, v125, v124
	v_mov_b32_e32 v125, 0x3d9d89d9
	v_cndmask_b32_e64 v125, v138, v125, s[6:7]
	v_fma_f32 v124, v125, v124, -v24
	v_cvt_pk_bf16_f32 v124, v124, s0
	ds_write_b16 v0, v124 offset:12480
	v_add_f32_e32 v124, v22, v24
	v_add_f32_e32 v124, v124, v26
	v_add_f32_e32 v124, v124, v29
	v_add_f32_e32 v124, v124, v33
	v_add_f32_e32 v124, v124, v36
	v_add_f32_e32 v124, v124, v39
	v_add_f32_e32 v124, v124, v32
	v_add_f32_e32 v124, v124, v35
	v_add_f32_e32 v124, v124, v38
	v_add_f32_e32 v124, v124, v41
	v_add_f32_e32 v124, v124, v43
	v_add_f32_e32 v124, v124, v46
	v_add_f32_e32 v124, v124, v49
	v_add_f32_e32 v124, v124, v115
	v_mov_b32_e32 v125, 0x3d924925
	v_add_f32_e32 v124, v124, v122
	v_cndmask_b32_e64 v125, v138, v125, s[6:7]
	v_fma_f32 v124, v125, v124, -v22
	v_cvt_pk_bf16_f32 v124, v124, s0
	ds_write_b16 v0, v124 offset:13520
	v_add_f32_e32 v124, v20, v22
	v_add_f32_e32 v124, v124, v24
	v_add_f32_e32 v124, v124, v26
	v_add_f32_e32 v124, v124, v29
	v_add_f32_e32 v124, v124, v33
	v_add_f32_e32 v124, v124, v36
	v_add_f32_e32 v124, v124, v39
	v_add_f32_e32 v124, v124, v32
	v_add_f32_e32 v124, v124, v35
	v_add_f32_e32 v124, v124, v38
	v_add_f32_e32 v124, v124, v41
	v_add_f32_e32 v124, v124, v43
	v_add_f32_e32 v124, v124, v46
	v_add_f32_e32 v124, v124, v49
	v_mov_b32_e32 v125, 0x3d888889
	v_add_f32_e32 v124, v124, v115
	v_cndmask_b32_e64 v125, v138, v125, s[6:7]
	v_fma_f32 v124, v125, v124, -v20
	v_cvt_pk_bf16_f32 v124, v124, s0
	ds_write_b16 v0, v124 offset:14560
	v_add_f32_e32 v124, v64, v20
	v_add_f32_e32 v124, v124, v22
	v_add_f32_e32 v124, v124, v24
	v_add_f32_e32 v124, v124, v26
	v_add_f32_e32 v124, v124, v29
	v_add_f32_e32 v124, v124, v33
	v_add_f32_e32 v124, v124, v36
	v_add_f32_e32 v124, v124, v39
	v_add_f32_e32 v124, v124, v32
	v_add_f32_e32 v124, v124, v35
	v_add_f32_e32 v124, v124, v38
	v_add_f32_e32 v124, v124, v41
	v_add_f32_e32 v124, v124, v43
	v_add_f32_e32 v124, v124, v46
	v_add_f32_e32 v124, v124, v49
	s_mov_b32 s4, 0x3d800000
	v_fma_f32 v124, v124, s4, -v64
	v_cvt_pk_bf16_f32 v124, v124, s0
	ds_write_b16 v0, v124 offset:15600
	v_add_f32_e32 v124, v62, v64
	v_add_f32_e32 v124, v124, v20
	v_add_f32_e32 v124, v124, v22
	v_add_f32_e32 v124, v124, v24
	v_add_f32_e32 v124, v124, v26
	v_add_f32_e32 v124, v124, v29
	v_add_f32_e32 v124, v124, v33
	v_add_f32_e32 v124, v124, v36
	v_add_f32_e32 v124, v124, v39
	v_add_f32_e32 v124, v124, v32
	v_add_f32_e32 v124, v124, v35
	v_add_f32_e32 v124, v124, v38
	v_add_f32_e32 v124, v124, v41
	v_add_f32_e32 v124, v124, v43
	v_add_f32_e32 v124, v124, v46
	v_fma_f32 v124, v124, s4, -v62
	v_cvt_pk_bf16_f32 v124, v124, s0
	ds_write_b16 v0, v124 offset:16640
	v_add_f32_e32 v124, v65, v62
	v_add_f32_e32 v124, v124, v64
	v_add_f32_e32 v124, v124, v20
	v_add_f32_e32 v124, v124, v22
	v_add_f32_e32 v124, v124, v24
	v_add_f32_e32 v124, v124, v26
	v_add_f32_e32 v124, v124, v29
	v_add_f32_e32 v124, v124, v33
	v_add_f32_e32 v124, v124, v36
	v_add_f32_e32 v124, v124, v39
	v_add_f32_e32 v124, v124, v32
	v_add_f32_e32 v124, v124, v35
	v_add_f32_e32 v124, v124, v38
	v_add_f32_e32 v124, v124, v41
	v_add_f32_e32 v124, v124, v43
	v_fma_f32 v124, v124, s4, -v65
	v_cvt_pk_bf16_f32 v124, v124, s0
	ds_write_b16 v0, v124 offset:17680
	v_add_f32_e32 v124, v63, v65
	v_add_f32_e32 v124, v124, v62
	v_add_f32_e32 v124, v124, v64
	v_add_f32_e32 v124, v124, v20
	v_add_f32_e32 v124, v124, v22
	v_add_f32_e32 v124, v124, v24
	v_add_f32_e32 v124, v124, v26
	v_add_f32_e32 v124, v124, v29
	v_add_f32_e32 v124, v124, v33
	v_add_f32_e32 v124, v124, v36
	v_add_f32_e32 v124, v124, v39
	v_add_f32_e32 v124, v124, v32
	v_add_f32_e32 v124, v124, v35
	v_add_f32_e32 v124, v124, v38
	v_add_f32_e32 v124, v124, v41
	v_fma_f32 v124, v124, s4, -v63
	v_cvt_pk_bf16_f32 v124, v124, s0
	ds_write_b16 v0, v124 offset:18720
	v_add_f32_e32 v124, v61, v63
	v_add_f32_e32 v124, v124, v65
	v_add_f32_e32 v124, v124, v62
	v_add_f32_e32 v124, v124, v64
	v_add_f32_e32 v124, v124, v20
	v_add_f32_e32 v124, v124, v22
	v_add_f32_e32 v124, v124, v24
	v_add_f32_e32 v124, v124, v26
	v_add_f32_e32 v124, v124, v29
	v_add_f32_e32 v124, v124, v33
	v_add_f32_e32 v124, v124, v36
	v_add_f32_e32 v124, v124, v39
	v_add_f32_e32 v124, v124, v32
	v_add_f32_e32 v124, v124, v35
	v_add_f32_e32 v124, v124, v38
	v_fma_f32 v124, v124, s4, -v61
	v_cvt_pk_bf16_f32 v124, v124, s0
	ds_write_b16 v0, v124 offset:19760
	v_add_f32_e32 v124, v60, v61
	v_add_f32_e32 v124, v124, v63
	v_add_f32_e32 v124, v124, v65
	v_add_f32_e32 v124, v124, v62
	v_add_f32_e32 v124, v124, v64
	v_add_f32_e32 v124, v124, v20
	v_add_f32_e32 v124, v124, v22
	v_add_f32_e32 v124, v124, v24
	v_add_f32_e32 v124, v124, v26
	v_add_f32_e32 v124, v124, v29
	v_add_f32_e32 v124, v124, v33
	v_add_f32_e32 v124, v124, v36
	v_add_f32_e32 v124, v124, v39
	v_add_f32_e32 v124, v124, v32
	v_add_f32_e32 v124, v124, v35
	v_fma_f32 v124, v124, s4, -v60
	v_cvt_pk_bf16_f32 v124, v124, s0
	ds_write_b16 v0, v124 offset:20800
	v_add_f32_e32 v124, v59, v60
	v_add_f32_e32 v124, v124, v61
	v_add_f32_e32 v124, v124, v63
	v_add_f32_e32 v124, v124, v65
	v_add_f32_e32 v124, v124, v62
	v_add_f32_e32 v124, v124, v64
	v_add_f32_e32 v124, v124, v20
	v_add_f32_e32 v124, v124, v22
	v_add_f32_e32 v124, v124, v24
	v_add_f32_e32 v124, v124, v26
	v_add_f32_e32 v124, v124, v29
	v_add_f32_e32 v124, v124, v33
	v_add_f32_e32 v124, v124, v36
	v_add_f32_e32 v124, v124, v39
	v_add_f32_e32 v124, v124, v32
	v_fma_f32 v124, v124, s4, -v59
	v_cvt_pk_bf16_f32 v124, v124, s0
	ds_write_b16 v0, v124 offset:21840
	v_add_f32_e32 v124, v58, v59
	v_add_f32_e32 v124, v124, v60
	v_add_f32_e32 v124, v124, v61
	v_add_f32_e32 v124, v124, v63
	v_add_f32_e32 v124, v124, v65
	v_add_f32_e32 v124, v124, v62
	v_add_f32_e32 v124, v124, v64
	v_add_f32_e32 v124, v124, v20
	v_add_f32_e32 v124, v124, v22
	v_add_f32_e32 v124, v124, v24
	v_add_f32_e32 v124, v124, v26
	v_add_f32_e32 v124, v124, v29
	v_add_f32_e32 v124, v124, v33
	v_add_f32_e32 v124, v124, v36
	v_add_f32_e32 v124, v124, v39
	v_fma_f32 v124, v124, s4, -v58
	v_cvt_pk_bf16_f32 v124, v124, s0
	ds_write_b16 v0, v124 offset:22880
	v_add_f32_e32 v124, v56, v58
	v_add_f32_e32 v124, v124, v59
	v_add_f32_e32 v124, v124, v60
	v_add_f32_e32 v124, v124, v61
	v_add_f32_e32 v124, v124, v63
	v_add_f32_e32 v124, v124, v65
	v_add_f32_e32 v124, v124, v62
	v_add_f32_e32 v124, v124, v64
	v_add_f32_e32 v124, v124, v20
	v_add_f32_e32 v124, v124, v22
	v_add_f32_e32 v124, v124, v24
	v_add_f32_e32 v124, v124, v26
	v_add_f32_e32 v124, v124, v29
	v_add_f32_e32 v124, v124, v33
	v_add_f32_e32 v124, v124, v36
	v_fma_f32 v124, v124, s4, -v56
	v_cvt_pk_bf16_f32 v124, v124, s0
	ds_write_b16 v0, v124 offset:23920
	v_add_f32_e32 v124, v54, v56
	v_add_f32_e32 v124, v124, v58
	v_add_f32_e32 v124, v124, v59
	v_add_f32_e32 v124, v124, v60
	v_add_f32_e32 v124, v124, v61
	v_add_f32_e32 v124, v124, v63
	v_add_f32_e32 v124, v124, v65
	v_add_f32_e32 v124, v124, v62
	v_add_f32_e32 v124, v124, v64
	v_add_f32_e32 v124, v124, v20
	v_add_f32_e32 v124, v124, v22
	v_add_f32_e32 v124, v124, v24
	v_add_f32_e32 v124, v124, v26
	v_add_f32_e32 v124, v124, v29
	v_add_f32_e32 v124, v124, v33
	v_fma_f32 v124, v124, s4, -v54
	v_cvt_pk_bf16_f32 v124, v124, s0
	ds_write_b16 v0, v124 offset:24960
	v_add_f32_e32 v124, v57, v54
	v_add_f32_e32 v124, v124, v56
	v_add_f32_e32 v124, v124, v58
	v_add_f32_e32 v124, v124, v59
	v_add_f32_e32 v124, v124, v60
	v_add_f32_e32 v124, v124, v61
	v_add_f32_e32 v124, v124, v63
	v_add_f32_e32 v124, v124, v65
	v_add_f32_e32 v124, v124, v62
	v_add_f32_e32 v124, v124, v64
	v_add_f32_e32 v124, v124, v20
	v_add_f32_e32 v124, v124, v22
	v_add_f32_e32 v124, v124, v24
	v_add_f32_e32 v124, v124, v26
	v_add_f32_e32 v124, v124, v29
	v_fma_f32 v124, v124, s4, -v57
	v_cvt_pk_bf16_f32 v124, v124, s0
	ds_write_b16 v0, v124 offset:26000
	v_add_f32_e32 v124, v55, v57
	v_add_f32_e32 v124, v124, v54
	v_add_f32_e32 v124, v124, v56
	v_add_f32_e32 v124, v124, v58
	v_add_f32_e32 v124, v124, v59
	v_add_f32_e32 v124, v124, v60
	v_add_f32_e32 v124, v124, v61
	v_add_f32_e32 v124, v124, v63
	v_add_f32_e32 v124, v124, v65
	v_add_f32_e32 v124, v124, v62
	v_add_f32_e32 v124, v124, v64
	v_add_f32_e32 v124, v124, v20
	v_add_f32_e32 v124, v124, v22
	v_add_f32_e32 v124, v124, v24
	v_add_f32_e32 v124, v124, v26
	v_fma_f32 v124, v124, s4, -v55
	v_cvt_pk_bf16_f32 v124, v124, s0
	ds_write_b16 v0, v124 offset:27040
	v_add_f32_e32 v124, v53, v55
	v_add_f32_e32 v124, v124, v57
	v_add_f32_e32 v124, v124, v54
	v_add_f32_e32 v124, v124, v56
	v_add_f32_e32 v124, v124, v58
	v_add_f32_e32 v124, v124, v59
	v_add_f32_e32 v124, v124, v60
	v_add_f32_e32 v124, v124, v61
	v_add_f32_e32 v124, v124, v63
	v_add_f32_e32 v124, v124, v65
	v_add_f32_e32 v124, v124, v62
	v_add_f32_e32 v124, v124, v64
	v_add_f32_e32 v124, v124, v20
	v_add_f32_e32 v124, v124, v22
	v_add_f32_e32 v124, v124, v24
	v_fma_f32 v124, v124, s4, -v53
	v_cvt_pk_bf16_f32 v124, v124, s0
	ds_write_b16 v0, v124 offset:28080
	v_add_f32_e32 v124, v52, v53
	v_add_f32_e32 v124, v124, v55
	v_add_f32_e32 v124, v124, v57
	v_add_f32_e32 v124, v124, v54
	v_add_f32_e32 v124, v124, v56
	v_add_f32_e32 v124, v124, v58
	v_add_f32_e32 v124, v124, v59
	v_add_f32_e32 v124, v124, v60
	v_add_f32_e32 v124, v124, v61
	v_add_f32_e32 v124, v124, v63
	v_add_f32_e32 v124, v124, v65
	v_add_f32_e32 v124, v124, v62
	v_add_f32_e32 v124, v124, v64
	v_add_f32_e32 v124, v124, v20
	v_add_f32_e32 v124, v124, v22
	v_fma_f32 v124, v124, s4, -v52
	v_cvt_pk_bf16_f32 v124, v124, s0
	ds_write_b16 v0, v124 offset:29120
	v_add_f32_e32 v124, v51, v52
	v_add_f32_e32 v124, v124, v53
	v_add_f32_e32 v124, v124, v55
	v_add_f32_e32 v124, v124, v57
	v_add_f32_e32 v124, v124, v54
	v_add_f32_e32 v124, v124, v56
	v_add_f32_e32 v124, v124, v58
	v_add_f32_e32 v124, v124, v59
	v_add_f32_e32 v124, v124, v60
	v_add_f32_e32 v124, v124, v61
	v_add_f32_e32 v124, v124, v63
	v_add_f32_e32 v124, v124, v65
	v_add_f32_e32 v124, v124, v62
	v_add_f32_e32 v124, v124, v64
	v_add_f32_e32 v124, v124, v20
	v_fma_f32 v124, v124, s4, -v51
	v_cvt_pk_bf16_f32 v124, v124, s0
	ds_write_b16 v0, v124 offset:30160
	v_add_f32_e32 v124, v50, v51
	v_add_f32_e32 v124, v124, v52
	v_add_f32_e32 v124, v124, v53
	v_add_f32_e32 v124, v124, v55
	v_add_f32_e32 v124, v124, v57
	v_add_f32_e32 v124, v124, v54
	v_add_f32_e32 v124, v124, v56
	v_add_f32_e32 v124, v124, v58
	v_add_f32_e32 v124, v124, v59
	v_add_f32_e32 v124, v124, v60
	v_add_f32_e32 v124, v124, v61
	v_add_f32_e32 v124, v124, v63
	v_add_f32_e32 v124, v124, v65
	v_add_f32_e32 v124, v124, v62
	v_add_f32_e32 v124, v124, v64
	v_fma_f32 v124, v124, s4, -v50
	v_cvt_pk_bf16_f32 v124, v124, s0
	ds_write_b16 v0, v124 offset:31200
	v_add_f32_e32 v124, v47, v50
	v_add_f32_e32 v124, v124, v51
	v_add_f32_e32 v124, v124, v52
	v_add_f32_e32 v124, v124, v53
	v_add_f32_e32 v124, v124, v55
	v_add_f32_e32 v124, v124, v57
	v_add_f32_e32 v124, v124, v54
	v_add_f32_e32 v124, v124, v56
	v_add_f32_e32 v124, v124, v58
	v_add_f32_e32 v124, v124, v59
	v_add_f32_e32 v124, v124, v60
	v_add_f32_e32 v124, v124, v61
	v_add_f32_e32 v124, v124, v63
	v_add_f32_e32 v124, v124, v65
	v_add_f32_e32 v124, v124, v62
	v_fma_f32 v124, v124, s4, -v47
	v_cvt_pk_bf16_f32 v124, v124, s0
	ds_write_b16 v0, v124 offset:32240
	v_add_f32_e32 v124, v44, v47
	v_add_f32_e32 v124, v124, v50
	v_add_f32_e32 v124, v124, v51
	v_add_f32_e32 v124, v124, v52
	v_add_f32_e32 v124, v124, v53
	v_add_f32_e32 v124, v124, v55
	v_add_f32_e32 v124, v124, v57
	v_add_f32_e32 v124, v124, v54
	v_add_f32_e32 v124, v124, v56
	v_add_f32_e32 v124, v124, v58
	v_add_f32_e32 v124, v124, v59
	v_add_f32_e32 v124, v124, v60
	v_add_f32_e32 v124, v124, v61
	v_add_f32_e32 v124, v124, v63
	v_add_f32_e32 v124, v124, v65
	v_fma_f32 v124, v124, s4, -v44
	v_cvt_pk_bf16_f32 v124, v124, s0
	ds_write_b16 v0, v124 offset:33280
	v_add_f32_e32 v124, v48, v44
	v_add_f32_e32 v124, v124, v47
	v_add_f32_e32 v124, v124, v50
	v_add_f32_e32 v124, v124, v51
	v_add_f32_e32 v124, v124, v52
	v_add_f32_e32 v124, v124, v53
	v_add_f32_e32 v124, v124, v55
	v_add_f32_e32 v124, v124, v57
	v_add_f32_e32 v124, v124, v54
	v_add_f32_e32 v124, v124, v56
	v_add_f32_e32 v124, v124, v58
	v_add_f32_e32 v124, v124, v59
	v_add_f32_e32 v124, v124, v60
	v_add_f32_e32 v124, v124, v61
	v_add_f32_e32 v124, v124, v63
	v_fma_f32 v124, v124, s4, -v48
	v_cvt_pk_bf16_f32 v124, v124, s0
	ds_write_b16 v0, v124 offset:34320
	v_add_f32_e32 v124, v45, v48
	v_add_f32_e32 v124, v124, v44
	v_add_f32_e32 v124, v124, v47
	v_add_f32_e32 v124, v124, v50
	v_add_f32_e32 v124, v124, v51
	v_add_f32_e32 v124, v124, v52
	v_add_f32_e32 v124, v124, v53
	v_add_f32_e32 v124, v124, v55
	v_add_f32_e32 v124, v124, v57
	v_add_f32_e32 v124, v124, v54
	v_add_f32_e32 v124, v124, v56
	v_add_f32_e32 v124, v124, v58
	v_add_f32_e32 v124, v124, v59
	v_add_f32_e32 v124, v124, v60
	v_add_f32_e32 v124, v124, v61
	v_fma_f32 v124, v124, s4, -v45
	v_cvt_pk_bf16_f32 v124, v124, s0
	ds_write_b16 v0, v124 offset:35360
	v_add_f32_e32 v124, v42, v45
	v_add_f32_e32 v124, v124, v48
	v_add_f32_e32 v124, v124, v44
	v_add_f32_e32 v124, v124, v47
	v_add_f32_e32 v124, v124, v50
	v_add_f32_e32 v124, v124, v51
	v_add_f32_e32 v124, v124, v52
	v_add_f32_e32 v124, v124, v53
	v_add_f32_e32 v124, v124, v55
	v_add_f32_e32 v124, v124, v57
	v_add_f32_e32 v124, v124, v54
	v_add_f32_e32 v124, v124, v56
	v_add_f32_e32 v124, v124, v58
	v_add_f32_e32 v124, v124, v59
	v_add_f32_e32 v124, v124, v60
	v_fma_f32 v124, v124, s4, -v42
	v_cvt_pk_bf16_f32 v124, v124, s0
	ds_write_b16 v0, v124 offset:36400
	v_add_f32_e32 v124, v40, v42
	v_add_f32_e32 v124, v124, v45
	v_add_f32_e32 v124, v124, v48
	v_add_f32_e32 v124, v124, v44
	v_add_f32_e32 v124, v124, v47
	v_add_f32_e32 v124, v124, v50
	v_add_f32_e32 v124, v124, v51
	v_add_f32_e32 v124, v124, v52
	v_add_f32_e32 v124, v124, v53
	v_add_f32_e32 v124, v124, v55
	v_add_f32_e32 v124, v124, v57
	v_add_f32_e32 v124, v124, v54
	v_add_f32_e32 v124, v124, v56
	v_add_f32_e32 v124, v124, v58
	v_add_f32_e32 v124, v124, v59
	v_fma_f32 v124, v124, s4, -v40
	v_cvt_pk_bf16_f32 v124, v124, s0
	ds_write_b16 v0, v124 offset:37440
	v_add_f32_e32 v124, v37, v40
	v_add_f32_e32 v124, v124, v42
	v_add_f32_e32 v124, v124, v45
	v_add_f32_e32 v124, v124, v48
	v_add_f32_e32 v124, v124, v44
	v_add_f32_e32 v124, v124, v47
	v_add_f32_e32 v124, v124, v50
	v_add_f32_e32 v124, v124, v51
	v_add_f32_e32 v124, v124, v52
	v_add_f32_e32 v124, v124, v53
	v_add_f32_e32 v124, v124, v55
	v_add_f32_e32 v124, v124, v57
	v_add_f32_e32 v124, v124, v54
	v_add_f32_e32 v124, v124, v56
	v_add_f32_e32 v124, v124, v58
	v_fma_f32 v124, v124, s4, -v37
	v_cvt_pk_bf16_f32 v124, v124, s0
	ds_write_b16 v0, v124 offset:38480
	v_add_f32_e32 v124, v34, v37
	v_add_f32_e32 v124, v124, v40
	v_add_f32_e32 v124, v124, v42
	v_add_f32_e32 v124, v124, v45
	v_add_f32_e32 v124, v124, v48
	v_add_f32_e32 v124, v124, v44
	v_add_f32_e32 v124, v124, v47
	v_add_f32_e32 v124, v124, v50
	v_add_f32_e32 v124, v124, v51
	v_add_f32_e32 v124, v124, v52
	v_add_f32_e32 v124, v124, v53
	v_add_f32_e32 v124, v124, v55
	v_add_f32_e32 v124, v124, v57
	v_add_f32_e32 v124, v124, v54
	v_add_f32_e32 v124, v124, v56
	v_fma_f32 v124, v124, s4, -v34
	v_cvt_pk_bf16_f32 v124, v124, s0
	ds_write_b16 v0, v124 offset:39520
	v_add_f32_e32 v124, v30, v34
	v_add_f32_e32 v124, v124, v37
	v_add_f32_e32 v124, v124, v40
	v_add_f32_e32 v124, v124, v42
	v_add_f32_e32 v124, v124, v45
	v_add_f32_e32 v124, v124, v48
	v_add_f32_e32 v124, v124, v44
	v_add_f32_e32 v124, v124, v47
	v_add_f32_e32 v124, v124, v50
	v_add_f32_e32 v124, v124, v51
	v_add_f32_e32 v124, v124, v52
	v_add_f32_e32 v124, v124, v53
	v_add_f32_e32 v124, v124, v55
	v_add_f32_e32 v124, v124, v57
	v_add_f32_e32 v124, v124, v54
	v_fma_f32 v124, v124, s4, -v30
	v_cvt_pk_bf16_f32 v124, v124, s0
	ds_write_b16 v0, v124 offset:40560
	v_add_f32_e32 v124, v27, v30
	v_add_f32_e32 v124, v124, v34
	v_add_f32_e32 v124, v124, v37
	v_add_f32_e32 v124, v124, v40
	v_add_f32_e32 v124, v124, v42
	v_add_f32_e32 v124, v124, v45
	v_add_f32_e32 v124, v124, v48
	v_add_f32_e32 v124, v124, v44
	v_add_f32_e32 v124, v124, v47
	v_add_f32_e32 v124, v124, v50
	v_add_f32_e32 v124, v124, v51
	v_add_f32_e32 v124, v124, v52
	v_add_f32_e32 v124, v124, v53
	v_add_f32_e32 v124, v124, v55
	v_add_f32_e32 v124, v124, v57
	v_fma_f32 v124, v124, s4, -v27
	v_cvt_pk_bf16_f32 v124, v124, s0
	ds_write_b16 v0, v124 offset:41600
	v_add_f32_e32 v124, v31, v27
	v_add_f32_e32 v124, v124, v30
	v_add_f32_e32 v124, v124, v34
	v_add_f32_e32 v124, v124, v37
	v_add_f32_e32 v124, v124, v40
	v_add_f32_e32 v124, v124, v42
	v_add_f32_e32 v124, v124, v45
	v_add_f32_e32 v124, v124, v48
	v_add_f32_e32 v124, v124, v44
	v_add_f32_e32 v124, v124, v47
	v_add_f32_e32 v124, v124, v50
	v_add_f32_e32 v124, v124, v51
	v_add_f32_e32 v124, v124, v52
	v_add_f32_e32 v124, v124, v53
	v_add_f32_e32 v124, v124, v55
	v_fma_f32 v124, v124, s4, -v31
	v_cvt_pk_bf16_f32 v124, v124, s0
	ds_write_b16 v0, v124 offset:42640
	v_add_f32_e32 v124, v28, v31
	v_add_f32_e32 v124, v124, v27
	v_add_f32_e32 v124, v124, v30
	v_add_f32_e32 v124, v124, v34
	v_add_f32_e32 v124, v124, v37
	v_add_f32_e32 v124, v124, v40
	v_add_f32_e32 v124, v124, v42
	v_add_f32_e32 v124, v124, v45
	v_add_f32_e32 v124, v124, v48
	v_add_f32_e32 v124, v124, v44
	v_add_f32_e32 v124, v124, v47
	v_add_f32_e32 v124, v124, v50
	v_add_f32_e32 v124, v124, v51
	v_add_f32_e32 v124, v124, v52
	v_add_f32_e32 v124, v124, v53
	v_fma_f32 v124, v124, s4, -v28
	v_cvt_pk_bf16_f32 v124, v124, s0
	ds_write_b16 v0, v124 offset:43680
	v_add_f32_e32 v124, v25, v28
	v_add_f32_e32 v124, v124, v31
	v_add_f32_e32 v124, v124, v27
	v_add_f32_e32 v124, v124, v30
	v_add_f32_e32 v124, v124, v34
	v_add_f32_e32 v124, v124, v37
	v_add_f32_e32 v124, v124, v40
	v_add_f32_e32 v124, v124, v42
	v_add_f32_e32 v124, v124, v45
	v_add_f32_e32 v124, v124, v48
	v_add_f32_e32 v124, v124, v44
	v_add_f32_e32 v124, v124, v47
	v_add_f32_e32 v124, v124, v50
	v_add_f32_e32 v124, v124, v51
	v_add_f32_e32 v124, v124, v52
	v_fma_f32 v124, v124, s4, -v25
	v_cvt_pk_bf16_f32 v124, v124, s0
	ds_write_b16 v0, v124 offset:44720
	v_add_f32_e32 v124, v23, v25
	v_add_f32_e32 v124, v124, v28
	v_add_f32_e32 v124, v124, v31
	v_add_f32_e32 v124, v124, v27
	v_add_f32_e32 v124, v124, v30
	v_add_f32_e32 v124, v124, v34
	v_add_f32_e32 v124, v124, v37
	v_add_f32_e32 v124, v124, v40
	v_add_f32_e32 v124, v124, v42
	v_add_f32_e32 v124, v124, v45
	v_add_f32_e32 v124, v124, v48
	v_add_f32_e32 v124, v124, v44
	v_add_f32_e32 v124, v124, v47
	v_add_f32_e32 v124, v124, v50
	v_add_f32_e32 v124, v124, v51
	v_fma_f32 v124, v124, s4, -v23
	v_cvt_pk_bf16_f32 v124, v124, s0
	ds_write_b16 v0, v124 offset:45760
	v_add_f32_e32 v124, v21, v23
	v_add_f32_e32 v124, v124, v25
	v_add_f32_e32 v124, v124, v28
	v_add_f32_e32 v124, v124, v31
	v_add_f32_e32 v124, v124, v27
	v_add_f32_e32 v124, v124, v30
	v_add_f32_e32 v124, v124, v34
	v_add_f32_e32 v124, v124, v37
	v_add_f32_e32 v124, v124, v40
	v_add_f32_e32 v124, v124, v42
	v_add_f32_e32 v124, v124, v45
	v_add_f32_e32 v124, v124, v48
	v_add_f32_e32 v124, v124, v44
	v_add_f32_e32 v124, v124, v47
	v_add_f32_e32 v124, v124, v50
	v_fma_f32 v124, v124, s4, -v21
	v_cvt_pk_bf16_f32 v124, v124, s0
	ds_write_b16 v0, v124 offset:46800
	v_add_f32_e32 v124, v19, v21
	v_add_f32_e32 v124, v124, v23
	v_add_f32_e32 v124, v124, v25
	v_add_f32_e32 v124, v124, v28
	v_add_f32_e32 v124, v124, v31
	v_add_f32_e32 v124, v124, v27
	v_add_f32_e32 v124, v124, v30
	v_add_f32_e32 v124, v124, v34
	v_add_f32_e32 v124, v124, v37
	v_add_f32_e32 v124, v124, v40
	v_add_f32_e32 v124, v124, v42
	v_add_f32_e32 v124, v124, v45
	v_add_f32_e32 v124, v124, v48
	v_add_f32_e32 v124, v124, v44
	v_add_f32_e32 v124, v124, v47
	v_fma_f32 v124, v124, s4, -v19
	v_cvt_pk_bf16_f32 v124, v124, s0
	ds_write_b16 v0, v124 offset:47840
	v_add_f32_e32 v124, v18, v19
	v_add_f32_e32 v124, v124, v21
	v_add_f32_e32 v124, v124, v23
	v_add_f32_e32 v124, v124, v25
	v_add_f32_e32 v124, v124, v28
	v_add_f32_e32 v124, v124, v31
	v_add_f32_e32 v124, v124, v27
	v_add_f32_e32 v124, v124, v30
	v_add_f32_e32 v124, v124, v34
	v_add_f32_e32 v124, v124, v37
	v_add_f32_e32 v124, v124, v40
	v_add_f32_e32 v124, v124, v42
	v_add_f32_e32 v124, v124, v45
	v_add_f32_e32 v124, v124, v48
	v_add_f32_e32 v124, v124, v44
	v_fma_f32 v124, v124, s4, -v18
	v_cvt_pk_bf16_f32 v124, v124, s0
	ds_write_b16 v0, v124 offset:48880
	v_add_f32_e32 v124, v16, v18
	v_add_f32_e32 v124, v124, v19
	v_add_f32_e32 v124, v124, v21
	v_add_f32_e32 v124, v124, v23
	v_add_f32_e32 v124, v124, v25
	v_add_f32_e32 v124, v124, v28
	v_add_f32_e32 v124, v124, v31
	v_add_f32_e32 v124, v124, v27
	v_add_f32_e32 v124, v124, v30
	v_add_f32_e32 v124, v124, v34
	v_add_f32_e32 v124, v124, v37
	v_add_f32_e32 v124, v124, v40
	v_add_f32_e32 v124, v124, v42
	v_add_f32_e32 v124, v124, v45
	v_add_f32_e32 v124, v124, v48
	v_fma_f32 v124, v124, s4, -v16
	v_cvt_pk_bf16_f32 v124, v124, s0
	ds_write_b16 v0, v124 offset:49920
	v_add_f32_e32 v124, v14, v16
	v_add_f32_e32 v124, v124, v18
	v_add_f32_e32 v124, v124, v19
	v_add_f32_e32 v124, v124, v21
	v_add_f32_e32 v124, v124, v23
	v_add_f32_e32 v124, v124, v25
	v_add_f32_e32 v124, v124, v28
	v_add_f32_e32 v124, v124, v31
	v_add_f32_e32 v124, v124, v27
	v_add_f32_e32 v124, v124, v30
	v_add_f32_e32 v124, v124, v34
	v_add_f32_e32 v124, v124, v37
	v_add_f32_e32 v124, v124, v40
	v_add_f32_e32 v124, v124, v42
	v_add_f32_e32 v124, v124, v45
	v_fma_f32 v124, v124, s4, -v14
	v_cvt_pk_bf16_f32 v124, v124, s0
	ds_write_b16 v0, v124 offset:50960
	v_add_f32_e32 v124, v12, v14
	v_add_f32_e32 v124, v124, v16
	v_add_f32_e32 v124, v124, v18
	v_add_f32_e32 v124, v124, v19
	v_add_f32_e32 v124, v124, v21
	v_add_f32_e32 v124, v124, v23
	v_add_f32_e32 v124, v124, v25
	v_add_f32_e32 v124, v124, v28
	v_add_f32_e32 v124, v124, v31
	v_add_f32_e32 v124, v124, v27
	v_add_f32_e32 v124, v124, v30
	v_add_f32_e32 v124, v124, v34
	v_add_f32_e32 v124, v124, v37
	v_add_f32_e32 v124, v124, v40
	v_add_f32_e32 v124, v124, v42
	v_fma_f32 v124, v124, s4, -v12
	v_cvt_pk_bf16_f32 v124, v124, s0
	ds_write_b16 v0, v124 offset:52000
	v_add_f32_e32 v124, v9, v12
	v_add_f32_e32 v124, v124, v14
	v_add_f32_e32 v124, v124, v16
	v_add_f32_e32 v124, v124, v18
	v_add_f32_e32 v124, v124, v19
	v_add_f32_e32 v124, v124, v21
	v_add_f32_e32 v124, v124, v23
	v_add_f32_e32 v124, v124, v25
	v_add_f32_e32 v124, v124, v28
	v_add_f32_e32 v124, v124, v31
	v_add_f32_e32 v124, v124, v27
	v_add_f32_e32 v124, v124, v30
	v_add_f32_e32 v124, v124, v34
	v_add_f32_e32 v124, v124, v37
	v_add_f32_e32 v124, v124, v40
	v_fma_f32 v124, v124, s4, -v9
	v_cvt_pk_bf16_f32 v124, v124, s0
	ds_write_b16 v0, v124 offset:53040
	v_add_f32_e32 v124, v7, v9
	v_add_f32_e32 v124, v124, v12
	v_add_f32_e32 v124, v124, v14
	v_add_f32_e32 v124, v124, v16
	v_add_f32_e32 v124, v124, v18
	v_add_f32_e32 v124, v124, v19
	v_add_f32_e32 v124, v124, v21
	v_add_f32_e32 v124, v124, v23
	v_add_f32_e32 v124, v124, v25
	v_add_f32_e32 v124, v124, v28
	v_add_f32_e32 v124, v124, v31
	v_add_f32_e32 v124, v124, v27
	v_add_f32_e32 v124, v124, v30
	v_add_f32_e32 v124, v124, v34
	v_add_f32_e32 v124, v124, v37
	v_fma_f32 v124, v124, s4, -v7
	v_cvt_pk_bf16_f32 v124, v124, s0
	ds_write_b16 v0, v124 offset:54080
	v_add_f32_e32 v124, v5, v7
	v_add_f32_e32 v124, v124, v9
	v_add_f32_e32 v124, v124, v12
	v_add_f32_e32 v124, v124, v14
	v_add_f32_e32 v124, v124, v16
	v_add_f32_e32 v124, v124, v18
	v_add_f32_e32 v124, v124, v19
	v_add_f32_e32 v124, v124, v21
	v_add_f32_e32 v124, v124, v23
	v_add_f32_e32 v124, v124, v25
	v_add_f32_e32 v124, v124, v28
	v_add_f32_e32 v124, v124, v31
	v_add_f32_e32 v124, v124, v27
	v_add_f32_e32 v124, v124, v30
	v_add_f32_e32 v124, v124, v34
	v_fma_f32 v124, v124, s4, -v5
	v_cvt_pk_bf16_f32 v124, v124, s0
	ds_write_b16 v0, v124 offset:55120
	v_add_f32_e32 v124, v3, v5
	v_add_f32_e32 v124, v124, v7
	v_add_f32_e32 v124, v124, v9
	v_add_f32_e32 v124, v124, v12
	v_add_f32_e32 v124, v124, v14
	v_add_f32_e32 v124, v124, v16
	v_add_f32_e32 v124, v124, v18
	v_add_f32_e32 v124, v124, v19
	v_add_f32_e32 v124, v124, v21
	v_add_f32_e32 v124, v124, v23
	v_add_f32_e32 v124, v124, v25
	v_add_f32_e32 v124, v124, v28
	v_add_f32_e32 v124, v124, v31
	v_add_f32_e32 v124, v124, v27
	v_add_f32_e32 v124, v124, v30
	v_fma_f32 v124, v124, s4, -v3
	v_cvt_pk_bf16_f32 v124, v124, s0
	ds_write_b16 v0, v124 offset:56160
	v_add_f32_e32 v124, v17, v3
	v_add_f32_e32 v124, v124, v5
	v_add_f32_e32 v124, v124, v7
	v_add_f32_e32 v124, v124, v9
	v_add_f32_e32 v124, v124, v12
	v_add_f32_e32 v124, v124, v14
	v_add_f32_e32 v124, v124, v16
	v_add_f32_e32 v124, v124, v18
	v_add_f32_e32 v124, v124, v19
	v_add_f32_e32 v124, v124, v21
	v_add_f32_e32 v124, v124, v23
	v_add_f32_e32 v124, v124, v25
	v_add_f32_e32 v124, v124, v28
	v_add_f32_e32 v124, v124, v31
	v_add_f32_e32 v124, v124, v27
	v_fma_f32 v124, v124, s4, -v17
	v_cvt_pk_bf16_f32 v124, v124, s0
	ds_write_b16 v0, v124 offset:57200
	v_add_f32_e32 v124, v15, v17
	v_add_f32_e32 v124, v124, v3
	v_add_f32_e32 v124, v124, v5
	v_add_f32_e32 v124, v124, v7
	v_add_f32_e32 v124, v124, v9
	v_add_f32_e32 v124, v124, v12
	v_add_f32_e32 v124, v124, v14
	v_add_f32_e32 v124, v124, v16
	v_add_f32_e32 v124, v124, v18
	v_add_f32_e32 v124, v124, v19
	v_add_f32_e32 v124, v124, v21
	v_add_f32_e32 v124, v124, v23
	v_add_f32_e32 v124, v124, v25
	v_add_f32_e32 v124, v124, v28
	v_add_f32_e32 v124, v124, v31
	v_fma_f32 v124, v124, s4, -v15
	v_cvt_pk_bf16_f32 v124, v124, s0
	ds_write_b16 v0, v124 offset:58240
	v_add_f32_e32 v124, v13, v15
	v_add_f32_e32 v124, v124, v17
	v_add_f32_e32 v124, v124, v3
	v_add_f32_e32 v124, v124, v5
	v_add_f32_e32 v124, v124, v7
	v_add_f32_e32 v124, v124, v9
	v_add_f32_e32 v124, v124, v12
	v_add_f32_e32 v124, v124, v14
	v_add_f32_e32 v124, v124, v16
	v_add_f32_e32 v124, v124, v18
	v_add_f32_e32 v124, v124, v19
	v_add_f32_e32 v124, v124, v21
	v_add_f32_e32 v124, v124, v23
	v_add_f32_e32 v124, v124, v25
	v_add_f32_e32 v124, v124, v28
	v_fma_f32 v124, v124, s4, -v13
	v_cvt_pk_bf16_f32 v124, v124, s0
	ds_write_b16 v0, v124 offset:59280
	v_add_f32_e32 v124, v11, v13
	v_add_f32_e32 v124, v124, v15
	v_add_f32_e32 v124, v124, v17
	v_add_f32_e32 v124, v124, v3
	v_add_f32_e32 v124, v124, v5
	v_add_f32_e32 v124, v124, v7
	v_add_f32_e32 v124, v124, v9
	v_add_f32_e32 v124, v124, v12
	v_add_f32_e32 v124, v124, v14
	v_add_f32_e32 v124, v124, v16
	v_add_f32_e32 v124, v124, v18
	v_add_f32_e32 v124, v124, v19
	v_add_f32_e32 v124, v124, v21
	v_add_f32_e32 v124, v124, v23
	v_add_f32_e32 v124, v124, v25
	v_fma_f32 v124, v124, s4, -v11
	v_cvt_pk_bf16_f32 v124, v124, s0
	ds_write_b16 v0, v124 offset:60320
	v_add_f32_e32 v124, v10, v11
	v_add_f32_e32 v124, v124, v13
	v_add_f32_e32 v124, v124, v15
	v_add_f32_e32 v124, v124, v17
	v_add_f32_e32 v124, v124, v3
	v_add_f32_e32 v124, v124, v5
	v_add_f32_e32 v124, v124, v7
	v_add_f32_e32 v124, v124, v9
	v_add_f32_e32 v124, v124, v12
	v_add_f32_e32 v124, v124, v14
	v_add_f32_e32 v124, v124, v16
	v_add_f32_e32 v124, v124, v18
	v_add_f32_e32 v124, v124, v19
	v_add_f32_e32 v124, v124, v21
	v_add_f32_e32 v124, v124, v23
	v_fma_f32 v124, v124, s4, -v10
	v_cvt_pk_bf16_f32 v124, v124, s0
	ds_write_b16 v0, v124 offset:61360
	v_add_f32_e32 v124, v8, v10
	v_add_f32_e32 v124, v124, v11
	v_add_f32_e32 v124, v124, v13
	v_add_f32_e32 v124, v124, v15
	v_add_f32_e32 v124, v124, v17
	v_add_f32_e32 v124, v124, v3
	v_add_f32_e32 v124, v124, v5
	v_add_f32_e32 v124, v124, v7
	v_add_f32_e32 v124, v124, v9
	v_add_f32_e32 v124, v124, v12
	v_add_f32_e32 v124, v124, v14
	v_add_f32_e32 v124, v124, v16
	v_add_f32_e32 v124, v124, v18
	v_add_f32_e32 v124, v124, v19
	v_add_f32_e32 v124, v124, v21
	v_fma_f32 v124, v124, s4, -v8
	v_cvt_pk_bf16_f32 v124, v124, s0
	ds_write_b16 v0, v124 offset:62400
	v_add_f32_e32 v124, v6, v8
	v_add_f32_e32 v124, v124, v10
	v_add_f32_e32 v124, v124, v11
	v_add_f32_e32 v124, v124, v13
	v_add_f32_e32 v124, v124, v15
	v_add_f32_e32 v124, v124, v17
	v_add_f32_e32 v124, v124, v3
	v_add_f32_e32 v124, v124, v5
	v_add_f32_e32 v124, v124, v7
	v_add_f32_e32 v124, v124, v9
	v_add_f32_e32 v124, v124, v12
	v_add_f32_e32 v124, v124, v14
	v_add_f32_e32 v124, v124, v16
	v_add_f32_e32 v124, v124, v18
	v_add_f32_e32 v124, v124, v19
	v_fma_f32 v124, v124, s4, -v6
	v_cvt_pk_bf16_f32 v124, v124, s0
	ds_write_b16 v0, v124 offset:63440
	v_add_f32_e32 v124, v4, v6
	v_add_f32_e32 v124, v124, v8
	v_add_f32_e32 v124, v124, v10
	v_add_f32_e32 v124, v124, v11
	v_add_f32_e32 v124, v124, v13
	v_add_f32_e32 v124, v124, v15
	v_add_f32_e32 v124, v124, v17
	v_add_f32_e32 v124, v124, v3
	v_add_f32_e32 v124, v124, v5
	v_add_f32_e32 v124, v124, v7
	v_add_f32_e32 v124, v124, v9
	v_add_f32_e32 v124, v124, v12
	v_add_f32_e32 v124, v124, v14
	v_add_f32_e32 v124, v124, v16
	v_add_f32_e32 v124, v124, v18
	v_fma_f32 v124, v124, s4, -v4
	v_cvt_pk_bf16_f32 v124, v124, s0
	ds_write_b16 v0, v124 offset:64480
	v_add_f32_e32 v124, v2, v4
	v_add_f32_e32 v124, v124, v6
	v_add_f32_e32 v124, v124, v8
	v_add_f32_e32 v124, v124, v10
	v_add_f32_e32 v124, v124, v11
	v_add_f32_e32 v124, v124, v13
	v_add_f32_e32 v124, v124, v15
	v_add_f32_e32 v124, v124, v17
	v_add_f32_e32 v124, v124, v3
	v_add_f32_e32 v124, v124, v5
	v_add_f32_e32 v124, v124, v7
	v_add_f32_e32 v124, v124, v9
	v_add_f32_e32 v124, v124, v12
	v_add_f32_e32 v124, v124, v14
	v_add_f32_e32 v124, v124, v16
	v_mul_f32_e32 v137, 0x3d800000, v124
	s_cbranch_execz .LBB0_593
	s_branch .LBB0_594

.LBB0_593:
	v_mov_b32_e32 v125, 0x3e800000
	v_cndmask_b32_e64 v124, v125, 1.0, s[6:7]
	v_fma_f32 v123, v124, v123, -v49
	v_cvt_pk_bf16_f32 v123, v123, s0
	ds_write_b16 v0, v123
	v_add_f32_e32 v123, v46, v49
	v_add_f32_e32 v123, v123, v115
	v_add_f32_e32 v122, v123, v122
	v_cndmask_b32_e64 v123, v125, 0.5, s[6:7]
	v_fma_f32 v122, v123, v122, -v46
	v_cvt_pk_bf16_f32 v122, v122, s0
	ds_write_b16 v0, v122 offset:1040
	v_add_f32_e32 v122, v43, v46
	v_add_f32_e32 v122, v122, v49
	v_add_f32_e32 v115, v122, v115
	v_mov_b32_e32 v122, 0x3eaaaaab
	v_cndmask_b32_e64 v122, v125, v122, s[6:7]
	v_fma_f32 v115, v122, v115, -v43
	v_cvt_pk_bf16_f32 v115, v115, s0
	ds_write_b16 v0, v115 offset:2080
	v_add_f32_e32 v115, v41, v43
	v_add_f32_e32 v115, v115, v46
	v_add_f32_e32 v115, v115, v49
	v_fma_f32 v115, v115, s97, -v41
	v_cvt_pk_bf16_f32 v115, v115, s0
	ds_write_b16 v0, v115 offset:3120
	v_add_f32_e32 v115, v38, v41
	v_add_f32_e32 v115, v115, v43
	v_add_f32_e32 v115, v115, v46
	v_fma_f32 v115, v115, s97, -v38
	v_cvt_pk_bf16_f32 v115, v115, s0
	ds_write_b16 v0, v115 offset:4160
	v_add_f32_e32 v115, v35, v38
	v_add_f32_e32 v115, v115, v41
	v_add_f32_e32 v115, v115, v43
	v_fma_f32 v115, v115, s97, -v35
	v_cvt_pk_bf16_f32 v115, v115, s0
	ds_write_b16 v0, v115 offset:5200
	v_add_f32_e32 v115, v32, v35
	v_add_f32_e32 v115, v115, v38
	v_add_f32_e32 v115, v115, v41
	v_fma_f32 v115, v115, s97, -v32
	v_cvt_pk_bf16_f32 v115, v115, s0
	ds_write_b16 v0, v115 offset:6240
	v_add_f32_e32 v115, v39, v32
	v_add_f32_e32 v115, v115, v35
	v_add_f32_e32 v115, v115, v38
	v_fma_f32 v115, v115, s97, -v39
	v_cvt_pk_bf16_f32 v115, v115, s0
	ds_write_b16 v0, v115 offset:7280
	v_add_f32_e32 v115, v36, v39
	v_add_f32_e32 v115, v115, v32
	v_add_f32_e32 v115, v115, v35
	v_fma_f32 v115, v115, s97, -v36
	v_cvt_pk_bf16_f32 v115, v115, s0
	ds_write_b16 v0, v115 offset:8320
	v_add_f32_e32 v115, v33, v36
	v_add_f32_e32 v115, v115, v39
	v_add_f32_e32 v115, v115, v32
	v_fma_f32 v115, v115, s97, -v33
	v_cvt_pk_bf16_f32 v115, v115, s0
	ds_write_b16 v0, v115 offset:9360
	v_add_f32_e32 v115, v29, v33
	v_add_f32_e32 v115, v115, v36
	v_add_f32_e32 v115, v115, v39
	v_fma_f32 v115, v115, s97, -v29
	v_cvt_pk_bf16_f32 v115, v115, s0
	ds_write_b16 v0, v115 offset:10400
	v_add_f32_e32 v115, v26, v29
	v_add_f32_e32 v115, v115, v33
	v_add_f32_e32 v115, v115, v36
	v_fma_f32 v115, v115, s97, -v26
	v_cvt_pk_bf16_f32 v115, v115, s0
	ds_write_b16 v0, v115 offset:11440
	v_add_f32_e32 v115, v24, v26
	v_add_f32_e32 v115, v115, v29
	v_add_f32_e32 v115, v115, v33
	v_fma_f32 v115, v115, s97, -v24
	v_cvt_pk_bf16_f32 v115, v115, s0
	ds_write_b16 v0, v115 offset:12480
	v_add_f32_e32 v115, v22, v24
	v_add_f32_e32 v115, v115, v26
	v_add_f32_e32 v115, v115, v29
	v_fma_f32 v115, v115, s97, -v22
	v_cvt_pk_bf16_f32 v115, v115, s0
	ds_write_b16 v0, v115 offset:13520
	v_add_f32_e32 v115, v20, v22
	v_add_f32_e32 v115, v115, v24
	v_add_f32_e32 v115, v115, v26
	v_fma_f32 v115, v115, s97, -v20
	v_cvt_pk_bf16_f32 v115, v115, s0
	ds_write_b16 v0, v115 offset:14560
	v_add_f32_e32 v115, v64, v20
	v_add_f32_e32 v115, v115, v22
	v_add_f32_e32 v115, v115, v24
	v_fma_f32 v115, v115, s97, -v64
	v_cvt_pk_bf16_f32 v115, v115, s0
	ds_write_b16 v0, v115 offset:15600
	v_add_f32_e32 v115, v62, v64
	v_add_f32_e32 v115, v115, v20
	v_add_f32_e32 v115, v115, v22
	v_fma_f32 v115, v115, s97, -v62
	v_cvt_pk_bf16_f32 v115, v115, s0
	ds_write_b16 v0, v115 offset:16640
	v_add_f32_e32 v115, v65, v62
	v_add_f32_e32 v115, v115, v64
	v_add_f32_e32 v115, v115, v20
	v_fma_f32 v115, v115, s97, -v65
	v_cvt_pk_bf16_f32 v115, v115, s0
	ds_write_b16 v0, v115 offset:17680
	v_add_f32_e32 v115, v63, v65
	v_add_f32_e32 v115, v115, v62
	v_add_f32_e32 v115, v115, v64
	v_fma_f32 v115, v115, s97, -v63
	v_cvt_pk_bf16_f32 v115, v115, s0
	ds_write_b16 v0, v115 offset:18720
	v_add_f32_e32 v115, v61, v63
	v_add_f32_e32 v115, v115, v65
	v_add_f32_e32 v115, v115, v62
	v_fma_f32 v115, v115, s97, -v61
	v_cvt_pk_bf16_f32 v115, v115, s0
	ds_write_b16 v0, v115 offset:19760
	v_add_f32_e32 v115, v60, v61
	v_add_f32_e32 v115, v115, v63
	v_add_f32_e32 v115, v115, v65
	v_fma_f32 v115, v115, s97, -v60
	v_cvt_pk_bf16_f32 v115, v115, s0
	ds_write_b16 v0, v115 offset:20800
	v_add_f32_e32 v115, v59, v60
	v_add_f32_e32 v115, v115, v61
	v_add_f32_e32 v115, v115, v63
	v_fma_f32 v115, v115, s97, -v59
	v_cvt_pk_bf16_f32 v115, v115, s0
	ds_write_b16 v0, v115 offset:21840
	v_add_f32_e32 v115, v58, v59
	v_add_f32_e32 v115, v115, v60
	v_add_f32_e32 v115, v115, v61
	v_fma_f32 v115, v115, s97, -v58
	v_cvt_pk_bf16_f32 v115, v115, s0
	ds_write_b16 v0, v115 offset:22880
	v_add_f32_e32 v115, v56, v58
	v_add_f32_e32 v115, v115, v59
	v_add_f32_e32 v115, v115, v60
	v_fma_f32 v115, v115, s97, -v56
	v_cvt_pk_bf16_f32 v115, v115, s0
	ds_write_b16 v0, v115 offset:23920
	v_add_f32_e32 v115, v54, v56
	v_add_f32_e32 v115, v115, v58
	v_add_f32_e32 v115, v115, v59
	v_fma_f32 v115, v115, s97, -v54
	v_cvt_pk_bf16_f32 v115, v115, s0
	ds_write_b16 v0, v115 offset:24960
	v_add_f32_e32 v115, v57, v54
	v_add_f32_e32 v115, v115, v56
	v_add_f32_e32 v115, v115, v58
	v_fma_f32 v115, v115, s97, -v57
	v_cvt_pk_bf16_f32 v115, v115, s0
	ds_write_b16 v0, v115 offset:26000
	v_add_f32_e32 v115, v55, v57
	v_add_f32_e32 v115, v115, v54
	v_add_f32_e32 v115, v115, v56
	v_fma_f32 v115, v115, s97, -v55
	v_cvt_pk_bf16_f32 v115, v115, s0
	ds_write_b16 v0, v115 offset:27040
	v_add_f32_e32 v115, v53, v55
	v_add_f32_e32 v115, v115, v57
	v_add_f32_e32 v115, v115, v54
	v_fma_f32 v115, v115, s97, -v53
	v_cvt_pk_bf16_f32 v115, v115, s0
	ds_write_b16 v0, v115 offset:28080
	v_add_f32_e32 v115, v52, v53
	v_add_f32_e32 v115, v115, v55
	v_add_f32_e32 v115, v115, v57
	v_fma_f32 v115, v115, s97, -v52
	v_cvt_pk_bf16_f32 v115, v115, s0
	ds_write_b16 v0, v115 offset:29120
	v_add_f32_e32 v115, v51, v52
	v_add_f32_e32 v115, v115, v53
	v_add_f32_e32 v115, v115, v55
	v_fma_f32 v115, v115, s97, -v51
	v_cvt_pk_bf16_f32 v115, v115, s0
	ds_write_b16 v0, v115 offset:30160
	v_add_f32_e32 v115, v50, v51
	v_add_f32_e32 v115, v115, v52
	v_add_f32_e32 v115, v115, v53
	v_fma_f32 v115, v115, s97, -v50
	v_cvt_pk_bf16_f32 v115, v115, s0
	ds_write_b16 v0, v115 offset:31200
	v_add_f32_e32 v115, v47, v50
	v_add_f32_e32 v115, v115, v51
	v_add_f32_e32 v115, v115, v52
	v_fma_f32 v115, v115, s97, -v47
	v_cvt_pk_bf16_f32 v115, v115, s0
	ds_write_b16 v0, v115 offset:32240
	v_add_f32_e32 v115, v44, v47
	v_add_f32_e32 v115, v115, v50
	v_add_f32_e32 v115, v115, v51
	v_fma_f32 v115, v115, s97, -v44
	v_cvt_pk_bf16_f32 v115, v115, s0
	ds_write_b16 v0, v115 offset:33280
	v_add_f32_e32 v115, v48, v44
	v_add_f32_e32 v115, v115, v47
	v_add_f32_e32 v115, v115, v50
	v_fma_f32 v115, v115, s97, -v48
	v_cvt_pk_bf16_f32 v115, v115, s0
	ds_write_b16 v0, v115 offset:34320
	v_add_f32_e32 v115, v45, v48
	v_add_f32_e32 v115, v115, v44
	v_add_f32_e32 v115, v115, v47
	v_fma_f32 v115, v115, s97, -v45
	v_cvt_pk_bf16_f32 v115, v115, s0
	ds_write_b16 v0, v115 offset:35360
	v_add_f32_e32 v115, v42, v45
	v_add_f32_e32 v115, v115, v48
	v_add_f32_e32 v115, v115, v44
	v_fma_f32 v115, v115, s97, -v42
	v_cvt_pk_bf16_f32 v115, v115, s0
	ds_write_b16 v0, v115 offset:36400
	v_add_f32_e32 v115, v40, v42
	v_add_f32_e32 v115, v115, v45
	v_add_f32_e32 v115, v115, v48
	v_fma_f32 v115, v115, s97, -v40
	v_cvt_pk_bf16_f32 v115, v115, s0
	ds_write_b16 v0, v115 offset:37440
	v_add_f32_e32 v115, v37, v40
	v_add_f32_e32 v115, v115, v42
	v_add_f32_e32 v115, v115, v45
	v_fma_f32 v115, v115, s97, -v37
	v_cvt_pk_bf16_f32 v115, v115, s0
	ds_write_b16 v0, v115 offset:38480
	v_add_f32_e32 v115, v34, v37
	v_add_f32_e32 v115, v115, v40
	v_add_f32_e32 v115, v115, v42
	v_fma_f32 v115, v115, s97, -v34
	v_cvt_pk_bf16_f32 v115, v115, s0
	ds_write_b16 v0, v115 offset:39520
	v_add_f32_e32 v115, v30, v34
	v_add_f32_e32 v115, v115, v37
	v_add_f32_e32 v115, v115, v40
	v_fma_f32 v115, v115, s97, -v30
	v_cvt_pk_bf16_f32 v115, v115, s0
	ds_write_b16 v0, v115 offset:40560
	v_add_f32_e32 v115, v27, v30
	v_add_f32_e32 v115, v115, v34
	v_add_f32_e32 v115, v115, v37
	v_fma_f32 v115, v115, s97, -v27
	v_cvt_pk_bf16_f32 v115, v115, s0
	ds_write_b16 v0, v115 offset:41600
	v_add_f32_e32 v115, v31, v27
	v_add_f32_e32 v115, v115, v30
	v_add_f32_e32 v115, v115, v34
	v_fma_f32 v115, v115, s97, -v31
	v_cvt_pk_bf16_f32 v115, v115, s0
	ds_write_b16 v0, v115 offset:42640
	v_add_f32_e32 v115, v28, v31
	v_add_f32_e32 v115, v115, v27
	v_add_f32_e32 v115, v115, v30
	v_fma_f32 v115, v115, s97, -v28
	v_cvt_pk_bf16_f32 v115, v115, s0
	ds_write_b16 v0, v115 offset:43680
	v_add_f32_e32 v115, v25, v28
	v_add_f32_e32 v115, v115, v31
	v_add_f32_e32 v115, v115, v27
	v_fma_f32 v115, v115, s97, -v25
	v_cvt_pk_bf16_f32 v115, v115, s0
	ds_write_b16 v0, v115 offset:44720
	v_add_f32_e32 v115, v23, v25
	v_add_f32_e32 v115, v115, v28
	v_add_f32_e32 v115, v115, v31
	v_fma_f32 v115, v115, s97, -v23
	v_cvt_pk_bf16_f32 v115, v115, s0
	ds_write_b16 v0, v115 offset:45760
	v_add_f32_e32 v115, v21, v23
	v_add_f32_e32 v115, v115, v25
	v_add_f32_e32 v115, v115, v28
	v_fma_f32 v115, v115, s97, -v21
	v_cvt_pk_bf16_f32 v115, v115, s0
	ds_write_b16 v0, v115 offset:46800
	v_add_f32_e32 v115, v19, v21
	v_add_f32_e32 v115, v115, v23
	v_add_f32_e32 v115, v115, v25
	v_fma_f32 v115, v115, s97, -v19
	v_cvt_pk_bf16_f32 v115, v115, s0
	ds_write_b16 v0, v115 offset:47840
	v_add_f32_e32 v115, v18, v19
	v_add_f32_e32 v115, v115, v21
	v_add_f32_e32 v115, v115, v23
	v_fma_f32 v115, v115, s97, -v18
	v_cvt_pk_bf16_f32 v115, v115, s0
	ds_write_b16 v0, v115 offset:48880
	v_add_f32_e32 v115, v16, v18
	v_add_f32_e32 v115, v115, v19
	v_add_f32_e32 v115, v115, v21
	v_fma_f32 v115, v115, s97, -v16
	v_cvt_pk_bf16_f32 v115, v115, s0
	ds_write_b16 v0, v115 offset:49920
	v_add_f32_e32 v115, v14, v16
	v_add_f32_e32 v115, v115, v18
	v_add_f32_e32 v115, v115, v19
	v_fma_f32 v115, v115, s97, -v14
	v_cvt_pk_bf16_f32 v115, v115, s0
	ds_write_b16 v0, v115 offset:50960
	v_add_f32_e32 v115, v12, v14
	v_add_f32_e32 v115, v115, v16
	v_add_f32_e32 v115, v115, v18
	v_fma_f32 v115, v115, s97, -v12
	v_cvt_pk_bf16_f32 v115, v115, s0
	ds_write_b16 v0, v115 offset:52000
	v_add_f32_e32 v115, v9, v12
	v_add_f32_e32 v115, v115, v14
	v_add_f32_e32 v115, v115, v16
	v_fma_f32 v115, v115, s97, -v9
	v_cvt_pk_bf16_f32 v115, v115, s0
	ds_write_b16 v0, v115 offset:53040
	v_add_f32_e32 v115, v7, v9
	v_add_f32_e32 v115, v115, v12
	v_add_f32_e32 v115, v115, v14
	v_fma_f32 v115, v115, s97, -v7
	v_cvt_pk_bf16_f32 v115, v115, s0
	ds_write_b16 v0, v115 offset:54080
	v_add_f32_e32 v115, v5, v7
	v_add_f32_e32 v115, v115, v9
	v_add_f32_e32 v115, v115, v12
	v_fma_f32 v115, v115, s97, -v5
	v_cvt_pk_bf16_f32 v115, v115, s0
	ds_write_b16 v0, v115 offset:55120
	v_add_f32_e32 v115, v3, v5
	v_add_f32_e32 v115, v115, v7
	v_add_f32_e32 v115, v115, v9
	v_fma_f32 v115, v115, s97, -v3
	v_cvt_pk_bf16_f32 v115, v115, s0
	ds_write_b16 v0, v115 offset:56160
	v_add_f32_e32 v115, v17, v3
	v_add_f32_e32 v115, v115, v5
	v_add_f32_e32 v115, v115, v7
	v_fma_f32 v115, v115, s97, -v17
	v_cvt_pk_bf16_f32 v115, v115, s0
	ds_write_b16 v0, v115 offset:57200
	v_add_f32_e32 v115, v15, v17
	v_add_f32_e32 v115, v115, v3
	v_add_f32_e32 v115, v115, v5
	v_fma_f32 v115, v115, s97, -v15
	v_cvt_pk_bf16_f32 v115, v115, s0
	ds_write_b16 v0, v115 offset:58240
	v_add_f32_e32 v115, v13, v15
	v_add_f32_e32 v115, v115, v17
	v_add_f32_e32 v115, v115, v3
	v_fma_f32 v115, v115, s97, -v13
	v_cvt_pk_bf16_f32 v115, v115, s0
	ds_write_b16 v0, v115 offset:59280
	v_add_f32_e32 v115, v11, v13
	v_add_f32_e32 v115, v115, v15
	v_add_f32_e32 v115, v115, v17
	v_fma_f32 v115, v115, s97, -v11
	v_cvt_pk_bf16_f32 v115, v115, s0
	ds_write_b16 v0, v115 offset:60320
	v_add_f32_e32 v115, v10, v11
	v_add_f32_e32 v115, v115, v13
	v_add_f32_e32 v115, v115, v15
	v_fma_f32 v115, v115, s97, -v10
	v_cvt_pk_bf16_f32 v115, v115, s0
	ds_write_b16 v0, v115 offset:61360
	v_add_f32_e32 v115, v8, v10
	v_add_f32_e32 v115, v115, v11
	v_add_f32_e32 v115, v115, v13
	v_fma_f32 v115, v115, s97, -v8
	v_cvt_pk_bf16_f32 v115, v115, s0
	ds_write_b16 v0, v115 offset:62400
	v_add_f32_e32 v115, v6, v8
	v_add_f32_e32 v115, v115, v10
	v_add_f32_e32 v115, v115, v11
	v_fma_f32 v115, v115, s97, -v6
	v_cvt_pk_bf16_f32 v115, v115, s0
	ds_write_b16 v0, v115 offset:63440
	v_add_f32_e32 v115, v4, v6
	v_add_f32_e32 v115, v115, v8
	v_add_f32_e32 v115, v115, v10
	v_fma_f32 v115, v115, s97, -v4
	v_cvt_pk_bf16_f32 v115, v115, s0
	ds_write_b16 v0, v115 offset:64480
	v_add_f32_e32 v115, v2, v4
	v_add_f32_e32 v115, v115, v6
	v_add_f32_e32 v115, v115, v8
	v_mul_f32_e32 v137, 0x3e800000, v115

.LBB0_595:
	s_and_b64 vcc, exec, s[8:9]
	s_cbranch_vccz .LBB0_597
	v_cndmask_b32_e64 v115, 0.5, 1.0, s[6:7]
	v_fma_f32 v114, v115, v114, -v49
	v_cvt_pk_bf16_f32 v114, v114, s0
	ds_write_b16 v0, v114
	v_add_f32_e32 v114, 0, v46
	v_add_f32_e32 v49, v114, v49
	v_fma_f32 v49, v49, 0.5, -v46
	v_cvt_pk_bf16_f32 v49, v49, s0
	ds_write_b16 v0, v49 offset:1040
	v_add_f32_e32 v49, 0, v43
	v_add_f32_e32 v46, v49, v46
	v_fma_f32 v46, v46, 0.5, -v43
	v_cvt_pk_bf16_f32 v46, v46, s0
	ds_write_b16 v0, v46 offset:2080
	v_add_f32_e32 v46, 0, v41
	v_add_f32_e32 v43, v46, v43
	v_fma_f32 v43, v43, 0.5, -v41
	v_cvt_pk_bf16_f32 v43, v43, s0
	ds_write_b16 v0, v43 offset:3120
	v_add_f32_e32 v43, 0, v38
	v_add_f32_e32 v41, v43, v41
	v_fma_f32 v41, v41, 0.5, -v38
	v_cvt_pk_bf16_f32 v41, v41, s0
	ds_write_b16 v0, v41 offset:4160
	v_add_f32_e32 v41, 0, v35
	v_add_f32_e32 v38, v41, v38
	v_fma_f32 v38, v38, 0.5, -v35
	v_cvt_pk_bf16_f32 v38, v38, s0
	ds_write_b16 v0, v38 offset:5200
	v_add_f32_e32 v38, 0, v32
	v_add_f32_e32 v35, v38, v35
	v_fma_f32 v35, v35, 0.5, -v32
	v_cvt_pk_bf16_f32 v35, v35, s0
	ds_write_b16 v0, v35 offset:6240
	v_add_f32_e32 v35, 0, v39
	v_add_f32_e32 v32, v35, v32
	v_fma_f32 v32, v32, 0.5, -v39
	v_cvt_pk_bf16_f32 v32, v32, s0
	ds_write_b16 v0, v32 offset:7280
	v_add_f32_e32 v32, v36, v39
	v_fma_f32 v32, v32, 0.5, -v36
	v_cvt_pk_bf16_f32 v32, v32, s0
	ds_write_b16 v0, v32 offset:8320
	v_add_f32_e32 v32, v33, v36
	v_fma_f32 v32, v32, 0.5, -v33
	v_cvt_pk_bf16_f32 v32, v32, s0
	ds_write_b16 v0, v32 offset:9360
	v_add_f32_e32 v32, v29, v33
	v_fma_f32 v32, v32, 0.5, -v29
	v_cvt_pk_bf16_f32 v32, v32, s0
	ds_write_b16 v0, v32 offset:10400
	v_add_f32_e32 v32, 0, v26
	v_add_f32_e32 v29, v32, v29
	v_fma_f32 v29, v29, 0.5, -v26
	v_cvt_pk_bf16_f32 v29, v29, s0
	ds_write_b16 v0, v29 offset:11440
	v_add_f32_e32 v29, 0, v24
	v_add_f32_e32 v26, v29, v26
	v_fma_f32 v26, v26, 0.5, -v24
	v_cvt_pk_bf16_f32 v26, v26, s0
	ds_write_b16 v0, v26 offset:12480
	v_add_f32_e32 v26, 0, v22
	v_add_f32_e32 v24, v26, v24
	v_fma_f32 v24, v24, 0.5, -v22
	v_cvt_pk_bf16_f32 v24, v24, s0
	ds_write_b16 v0, v24 offset:13520
	v_add_f32_e32 v24, 0, v20
	v_add_f32_e32 v22, v24, v22
	v_fma_f32 v22, v22, 0.5, -v20
	v_cvt_pk_bf16_f32 v22, v22, s0
	ds_write_b16 v0, v22 offset:14560
	v_add_f32_e32 v22, 0, v64
	v_add_f32_e32 v20, v22, v20
	v_fma_f32 v20, v20, 0.5, -v64
	v_cvt_pk_bf16_f32 v20, v20, s0
	ds_write_b16 v0, v20 offset:15600
	v_add_f32_e32 v20, v62, v64
	v_fma_f32 v20, v20, 0.5, -v62
	v_cvt_pk_bf16_f32 v20, v20, s0
	ds_write_b16 v0, v20 offset:16640
	v_add_f32_e32 v20, v65, v62
	v_fma_f32 v20, v20, 0.5, -v65
	v_cvt_pk_bf16_f32 v20, v20, s0
	ds_write_b16 v0, v20 offset:17680
	v_add_f32_e32 v20, v63, v65
	v_fma_f32 v20, v20, 0.5, -v63
	v_cvt_pk_bf16_f32 v20, v20, s0
	ds_write_b16 v0, v20 offset:18720
	v_add_f32_e32 v20, v61, v63
	v_fma_f32 v20, v20, 0.5, -v61
	v_cvt_pk_bf16_f32 v20, v20, s0
	ds_write_b16 v0, v20 offset:19760
	v_add_f32_e32 v20, v60, v61
	v_fma_f32 v20, v20, 0.5, -v60
	v_cvt_pk_bf16_f32 v20, v20, s0
	ds_write_b16 v0, v20 offset:20800
	v_add_f32_e32 v20, v59, v60
	v_fma_f32 v20, v20, 0.5, -v59
	v_cvt_pk_bf16_f32 v20, v20, s0
	ds_write_b16 v0, v20 offset:21840
	v_add_f32_e32 v20, v58, v59
	v_fma_f32 v20, v20, 0.5, -v58
	v_cvt_pk_bf16_f32 v20, v20, s0
	ds_write_b16 v0, v20 offset:22880
	v_add_f32_e32 v20, v56, v58
	v_fma_f32 v20, v20, 0.5, -v56
	v_cvt_pk_bf16_f32 v20, v20, s0
	ds_write_b16 v0, v20 offset:23920
	v_add_f32_e32 v20, v54, v56
	v_fma_f32 v20, v20, 0.5, -v54
	v_cvt_pk_bf16_f32 v20, v20, s0
	ds_write_b16 v0, v20 offset:24960
	v_add_f32_e32 v20, v57, v54
	v_fma_f32 v20, v20, 0.5, -v57
	v_cvt_pk_bf16_f32 v20, v20, s0
	ds_write_b16 v0, v20 offset:26000
	v_add_f32_e32 v20, v55, v57
	v_fma_f32 v20, v20, 0.5, -v55
	v_cvt_pk_bf16_f32 v20, v20, s0
	ds_write_b16 v0, v20 offset:27040
	v_add_f32_e32 v20, v53, v55
	v_fma_f32 v20, v20, 0.5, -v53
	v_cvt_pk_bf16_f32 v20, v20, s0
	ds_write_b16 v0, v20 offset:28080
	v_add_f32_e32 v20, v52, v53
	v_fma_f32 v20, v20, 0.5, -v52
	v_cvt_pk_bf16_f32 v20, v20, s0
	ds_write_b16 v0, v20 offset:29120
	v_add_f32_e32 v20, v51, v52
	v_fma_f32 v20, v20, 0.5, -v51
	v_cvt_pk_bf16_f32 v20, v20, s0
	ds_write_b16 v0, v20 offset:30160
	v_add_f32_e32 v20, v50, v51
	v_fma_f32 v20, v20, 0.5, -v50
	v_cvt_pk_bf16_f32 v20, v20, s0
	ds_write_b16 v0, v20 offset:31200
	v_add_f32_e32 v20, v47, v50
	v_fma_f32 v20, v20, 0.5, -v47
	v_cvt_pk_bf16_f32 v20, v20, s0
	ds_write_b16 v0, v20 offset:32240
	v_add_f32_e32 v20, v44, v47
	v_fma_f32 v20, v20, 0.5, -v44
	v_cvt_pk_bf16_f32 v20, v20, s0
	ds_write_b16 v0, v20 offset:33280
	v_add_f32_e32 v20, v48, v44
	v_fma_f32 v20, v20, 0.5, -v48
	v_cvt_pk_bf16_f32 v20, v20, s0
	ds_write_b16 v0, v20 offset:34320
	v_add_f32_e32 v20, v45, v48
	v_fma_f32 v20, v20, 0.5, -v45
	v_cvt_pk_bf16_f32 v20, v20, s0
	ds_write_b16 v0, v20 offset:35360
	v_add_f32_e32 v20, v42, v45
	v_fma_f32 v20, v20, 0.5, -v42
	v_cvt_pk_bf16_f32 v20, v20, s0
	ds_write_b16 v0, v20 offset:36400
	v_add_f32_e32 v20, v40, v42
	v_fma_f32 v20, v20, 0.5, -v40
	v_cvt_pk_bf16_f32 v20, v20, s0
	ds_write_b16 v0, v20 offset:37440
	v_add_f32_e32 v20, v37, v40
	v_fma_f32 v20, v20, 0.5, -v37
	v_cvt_pk_bf16_f32 v20, v20, s0
	ds_write_b16 v0, v20 offset:38480
	v_add_f32_e32 v20, v34, v37
	v_fma_f32 v20, v20, 0.5, -v34
	v_cvt_pk_bf16_f32 v20, v20, s0
	ds_write_b16 v0, v20 offset:39520
	v_add_f32_e32 v20, v30, v34
	v_fma_f32 v20, v20, 0.5, -v30
	v_cvt_pk_bf16_f32 v20, v20, s0
	ds_write_b16 v0, v20 offset:40560
	v_add_f32_e32 v20, v27, v30
	v_fma_f32 v20, v20, 0.5, -v27
	v_cvt_pk_bf16_f32 v20, v20, s0
	ds_write_b16 v0, v20 offset:41600
	v_add_f32_e32 v20, v31, v27
	v_fma_f32 v20, v20, 0.5, -v31
	v_cvt_pk_bf16_f32 v20, v20, s0
	ds_write_b16 v0, v20 offset:42640
	v_add_f32_e32 v20, v28, v31
	v_fma_f32 v20, v20, 0.5, -v28
	v_cvt_pk_bf16_f32 v20, v20, s0
	ds_write_b16 v0, v20 offset:43680
	v_add_f32_e32 v20, v25, v28
	v_fma_f32 v20, v20, 0.5, -v25
	v_cvt_pk_bf16_f32 v20, v20, s0
	ds_write_b16 v0, v20 offset:44720
	v_add_f32_e32 v20, v23, v25
	v_fma_f32 v20, v20, 0.5, -v23
	v_cvt_pk_bf16_f32 v20, v20, s0
	ds_write_b16 v0, v20 offset:45760
	v_add_f32_e32 v20, v21, v23
	v_fma_f32 v20, v20, 0.5, -v21
	v_cvt_pk_bf16_f32 v20, v20, s0
	ds_write_b16 v0, v20 offset:46800
	v_add_f32_e32 v20, v19, v21
	v_fma_f32 v20, v20, 0.5, -v19
	v_cvt_pk_bf16_f32 v20, v20, s0
	ds_write_b16 v0, v20 offset:47840
	v_add_f32_e32 v20, 0, v18
	v_add_f32_e32 v19, v20, v19
	v_fma_f32 v19, v19, 0.5, -v18
	v_cvt_pk_bf16_f32 v19, v19, s0
	ds_write_b16 v0, v19 offset:48880
	v_add_f32_e32 v19, 0, v16
	v_add_f32_e32 v18, v19, v18
	v_fma_f32 v18, v18, 0.5, -v16
	v_cvt_pk_bf16_f32 v18, v18, s0
	ds_write_b16 v0, v18 offset:49920
	v_add_f32_e32 v18, 0, v14
	v_add_f32_e32 v16, v18, v16
	v_fma_f32 v16, v16, 0.5, -v14
	v_cvt_pk_bf16_f32 v16, v16, s0
	ds_write_b16 v0, v16 offset:50960
	v_add_f32_e32 v16, 0, v12
	v_add_f32_e32 v14, v16, v14
	v_fma_f32 v14, v14, 0.5, -v12
	v_cvt_pk_bf16_f32 v14, v14, s0
	ds_write_b16 v0, v14 offset:52000
	v_add_f32_e32 v14, 0, v9
	v_add_f32_e32 v12, v14, v12
	v_fma_f32 v12, v12, 0.5, -v9
	v_cvt_pk_bf16_f32 v12, v12, s0
	ds_write_b16 v0, v12 offset:53040
	v_add_f32_e32 v12, 0, v7
	v_add_f32_e32 v9, v12, v9
	v_fma_f32 v9, v9, 0.5, -v7
	v_cvt_pk_bf16_f32 v9, v9, s0
	ds_write_b16 v0, v9 offset:54080
	v_add_f32_e32 v9, 0, v5
	v_add_f32_e32 v7, v9, v7
	v_fma_f32 v7, v7, 0.5, -v5
	v_cvt_pk_bf16_f32 v7, v7, s0
	ds_write_b16 v0, v7 offset:55120
	v_add_f32_e32 v7, 0, v3
	v_add_f32_e32 v5, v7, v5
	v_fma_f32 v5, v5, 0.5, -v3
	v_cvt_pk_bf16_f32 v5, v5, s0
	ds_write_b16 v0, v5 offset:56160
	v_add_f32_e32 v5, 0, v17
	v_add_f32_e32 v3, v5, v3
	v_fma_f32 v3, v3, 0.5, -v17
	v_cvt_pk_bf16_f32 v3, v3, s0
	ds_write_b16 v0, v3 offset:57200
	v_add_f32_e32 v3, v15, v17
	v_fma_f32 v3, v3, 0.5, -v15
	v_cvt_pk_bf16_f32 v3, v3, s0
	ds_write_b16 v0, v3 offset:58240
	v_add_f32_e32 v3, v13, v15
	v_fma_f32 v3, v3, 0.5, -v13
	v_cvt_pk_bf16_f32 v3, v3, s0
	ds_write_b16 v0, v3 offset:59280
	v_add_f32_e32 v3, v11, v13
	v_fma_f32 v3, v3, 0.5, -v11
	v_cvt_pk_bf16_f32 v3, v3, s0
	ds_write_b16 v0, v3 offset:60320
	v_add_f32_e32 v3, v10, v11
	v_fma_f32 v3, v3, 0.5, -v10
	v_cvt_pk_bf16_f32 v3, v3, s0
	ds_write_b16 v0, v3 offset:61360
	v_add_f32_e32 v3, v8, v10
	v_fma_f32 v3, v3, 0.5, -v8
	v_cvt_pk_bf16_f32 v3, v3, s0
	ds_write_b16 v0, v3 offset:62400
	v_add_f32_e32 v3, v6, v8
	v_fma_f32 v3, v3, 0.5, -v6
	v_cvt_pk_bf16_f32 v3, v3, s0
	ds_write_b16 v0, v3 offset:63440
	v_add_f32_e32 v3, v4, v6
	v_fma_f32 v3, v3, 0.5, -v4
	v_cvt_pk_bf16_f32 v3, v3, s0
	ds_write_b16 v0, v3 offset:64480
	v_add_f32_e32 v3, v2, v4
	v_mul_f32_e32 v137, 0.5, v3
